# baseline (speedup 1.0000x reference)
_Z11lstm_kernelPKiPKhPKfS4_S4_Pf:
	s_load_dwordx4 s[12:15], s[0:1], 0x0
	v_readfirstlane_b32 s19, v0
	v_or_b32_e32 v3, 0x400, v0
	s_movk_i32 s4, 0x500
	s_lshr_b32 s7, s19, 6
	s_lshl_b32 s18, s2, 6
	s_mulk_i32 s2, 0x1400
	v_mov_b32_e32 v2, 0x4ff
	v_cmp_gt_u32_e32 vcc, s4, v3
	s_mul_hi_i32 s3, s18, 0x50
	s_waitcnt lgkmcnt(0)
	s_add_u32 s2, s12, s2
	v_cndmask_b32_e32 v2, v2, v3, vcc
	s_addc_u32 s3, s13, s3
	v_lshlrev_b32_e32 v1, 2, v0
	v_lshlrev_b32_e32 v4, 2, v2
	s_movk_i32 s4, 0x184
	v_or_b32_e32 v28, 0x200, v0
	global_load_dword v29, v1, s[2:3]
	global_load_dword v30, v1, s[2:3] offset:2048
	global_load_dword v2, v4, s[2:3]
	v_mov_b32_e32 v4, 0x383
	v_cmp_gt_u32_e32 vcc, s4, v0
	s_add_u32 s2, s14, 0x34000
	s_addc_u32 s3, s15, 0
	v_cndmask_b32_e32 v4, v4, v28, vcc
	v_lshlrev_b32_e32 v31, 4, v0
	v_lshlrev_b32_e32 v4, 4, v4
	global_load_dwordx4 v[6:9], v31, s[2:3]
	global_load_dwordx4 v[10:13], v4, s[2:3]
	v_and_b32_e32 v4, 0x7f, v0
	v_lshlrev_b32_e32 v18, 4, v4
	v_mov_b32_e32 v19, 0
	v_lshl_add_u64 v[4:5], s[14:15], 0, v[18:19]
	s_mov_b32 s2, 0x37000
	v_add_co_u32_e64 v4, s[2:3], s2, v4
	s_nop 1
	v_addc_co_u32_e64 v5, s[2:3], 0, v5, s[2:3]
	global_load_dwordx4 v[14:17], v[4:5], off offset:2112
	s_movk_i32 s22, 0x410
	s_movk_i32 s2, 0x4ff
	v_and_b32_e32 v4, 63, v0
	v_cmp_lt_u32_e64 s[2:3], s2, v3
	s_mul_i32 s5, s7, 0x6000
	s_mul_hi_u32 s4, s7, 0x6000
	s_add_u32 s8, s14, s5
	s_addc_u32 s9, s15, s4
	v_lshlrev_b32_e32 v210, 4, v4
	v_mov_b32_e32 v211, v19
	v_lshl_add_u64 v[20:21], s[8:9], 0, v[210:211]
	s_movk_i32 s4, 0x2000
	v_add_co_u32_e64 v22, s[4:5], s4, v20
	s_nop 1
	v_addc_co_u32_e64 v23, s[4:5], 0, v21, s[4:5]
	s_movk_i32 s4, 0x3000
	s_nop 0
	v_add_co_u32_e64 v24, s[4:5], s4, v20
	global_load_dwordx4 v[90:93], v[22:23], off offset:1024
	global_load_dwordx4 v[86:89], v[22:23], off offset:2048
	v_addc_co_u32_e64 v25, s[4:5], 0, v21, s[4:5]
	s_movk_i32 s4, 0x5000
	s_nop 0
	v_add_co_u32_e64 v26, s[4:5], s4, v20
	s_nop 1
	v_addc_co_u32_e64 v27, s[4:5], 0, v21, s[4:5]
	global_load_dwordx4 v[82:85], v[22:23], off offset:3072
	global_load_dwordx4 v[46:49], v[26:27], off
	global_load_dwordx4 v[42:45], v[26:27], off offset:1024
	global_load_dwordx4 v[38:41], v[26:27], off offset:2048
	global_load_dwordx4 v[94:97], v[24:25], off offset:-4096
	global_load_dwordx4 v[34:37], v[26:27], off offset:3072
	s_movk_i32 s4, 0x1000
	v_add_co_u32_e64 v22, s[4:5], s4, v20
	global_load_dwordx4 v[126:129], v210, s[8:9]
	global_load_dwordx4 v[122:125], v210, s[8:9] offset:1024
	global_load_dwordx4 v[118:121], v210, s[8:9] offset:2048
	global_load_dwordx4 v[114:117], v210, s[8:9] offset:3072
	v_addc_co_u32_e64 v23, s[4:5], 0, v21, s[4:5]
	global_load_dwordx4 v[110:113], v[22:23], off
	global_load_dwordx4 v[106:109], v[22:23], off offset:1024
	global_load_dwordx4 v[102:105], v[22:23], off offset:2048
	global_load_dwordx4 v[98:101], v[22:23], off offset:3072
	global_load_dwordx4 v[78:81], v[24:25], off
	global_load_dwordx4 v[74:77], v[24:25], off offset:1024
	global_load_dwordx4 v[70:73], v[24:25], off offset:2048
	global_load_dwordx4 v[66:69], v[24:25], off offset:3072
	s_movk_i32 s4, 0x4000
	v_add_co_u32_e64 v20, s[4:5], s4, v20
	v_mov_b32_e32 v5, 0x4000
	s_nop 0
	v_addc_co_u32_e64 v21, s[4:5], 0, v21, s[4:5]
	global_load_dwordx4 v[62:65], v[20:21], off
	global_load_dwordx4 v[58:61], v[20:21], off offset:1024
	global_load_dwordx4 v[54:57], v[20:21], off offset:2048
	global_load_dwordx4 v[50:53], v[20:21], off offset:3072
	s_waitcnt vmcnt(26)
	ds_write_b128 v31, v[6:9] offset:16384
	v_lshl_or_b32 v5, v28, 4, v5
	v_add_u32_e32 v6, 0x9840, v31
	v_cndmask_b32_e32 v5, v6, v5, vcc
	s_waitcnt vmcnt(25)
	ds_write_b128 v5, v[10:13]
	s_waitcnt vmcnt(24)
	ds_write_b128 v18, v[14:17] offset:36928
	v_mul_u32_u24_e32 v5, 0xccd, v0
	v_lshrrev_b32_e32 v5, 16, v5
	s_mov_b32 s5, 0xffffec
	v_mul_u32_u24_e32 v6, 0xccd, v28
	s_movk_i32 s4, 0x90
	v_mad_u32_u24 v8, v5, s5, v0
	v_lshlrev_b32_e32 v5, 2, v5
	v_lshrrev_b32_e32 v6, 16, v6
	v_mul_lo_u32 v7, v29, s4
	v_lshl_or_b32 v5, v8, 8, v5
	ds_write_b32 v5, v7 offset:30784
	v_mul_lo_u32 v196, v29, s22
	v_add_u32_e32 v197, 0x24e80, v5
	ds_write_b32 v197, v196
	v_mad_u32_u24 v7, v6, s5, v28
	v_lshlrev_b32_e32 v6, 2, v6
	v_mul_lo_u32 v5, v30, s4
	v_lshl_or_b32 v6, v7, 8, v6
	ds_write_b32 v6, v5 offset:30784
	v_mul_lo_u32 v198, v30, s22
	v_add_u32_e32 v199, 0x24e80, v6
	ds_write_b32 v199, v198
	s_and_saveexec_b64 s[4:5], s[2:3]
	s_xor_b64 s[2:3], exec, s[4:5]
	v_mov_b32_e32 v3, 0x9840
	v_lshl_add_u32 v5, v0, 2, v3
	s_andn2_saveexec_b64 s[2:3], s[2:3]
	v_mul_u32_u24_e32 v5, 0xccd, v3
	s_mov_b32 s4, 0xffffec
	v_mul_u32_u24_sdwa v6, v5, s4 dst_sel:DWORD dst_unused:UNUSED_PAD src0_sel:WORD_1 src1_sel:DWORD
	v_add_lshl_u32 v3, v6, v3, 8
	v_mov_b32_e32 v6, 2
	v_lshlrev_b32_sdwa v5, v6, v5 dst_sel:DWORD dst_unused:UNUSED_PAD src0_sel:DWORD src1_sel:WORD_1
	s_movk_i32 s4, 0x7840
	v_add3_u32 v5, v5, v3, s4
	s_or_b64 exec, exec, s[2:3]
	v_lshrrev_b32_e32 v3, 5, v4
	s_movk_i32 s2, 0x90
	s_lshl_b32 s6, s7, 10
	s_mulk_i32 s7, 0xfd00
	v_and_b32_e32 v182, 31, v0
	v_mul_lo_u32 v200, v2, s22
	v_mul_lo_u32 v2, v2, s2
	s_add_i32 s7, s6, s7
	v_lshlrev_b32_e32 v229, 6, v3
	ds_write_b32 v5, v2
	v_add_u32_e32 v201, 0x1d640, v5
	ds_write_b32 v201, v200
	v_lshlrev_b32_e32 v230, 4, v3
	v_lshlrev_b32_e32 v228, 2, v182
	v_or_b32_e32 v2, s7, v229
	s_waitcnt lgkmcnt(0)
	s_barrier
	s_cmpk_lt_u32 s19, 0x100
	s_cbranch_scc1 .Llight_path
	s_setprio 1
	s_mov_b32 s12, 0xbeb17218
	v_add_u32_e32 v3, 0x7800, v228
	ds_read2_b32 v[138:139], v3 offset0:16 offset1:48
	ds_read_b128 v[18:21], v2 offset:36928
	ds_read_b128 v[22:25], v2 offset:36944
	s_waitcnt lgkmcnt(2)
	v_add_u32_e32 v3, v230, v138
	ds_read_b128 v[26:29], v2 offset:36960
	ds_read_b128 v[30:33], v2 offset:36976
	ds_read_b128 v[142:145], v3 offset:16384
	ds_read_b128 v[130:133], v3 offset:16416
	ds_read_b128 v[154:157], v3 offset:16448
	ds_read_b128 v[134:137], v3 offset:16480
	ds_read_b128 v[248:251], v2 offset:37104
	ds_read_b128 v[244:247], v2 offset:37088
	ds_read_b128 v[240:243], v2 offset:37072
	ds_read_b128 v[236:239], v2 offset:37056
	s_waitcnt vmcnt(17) lgkmcnt(7)
	v_mfma_f32_32x32x16_bf16 v[18:33], v[94:97], v[142:145], v[18:33]
	s_waitcnt lgkmcnt(6)
	v_mfma_f32_32x32x16_bf16 v[18:33], v[90:93], v[130:133], v[18:33]
	s_waitcnt lgkmcnt(5)
	v_mfma_f32_32x32x16_bf16 v[18:33], v[86:89], v[154:157], v[18:33]
	s_waitcnt lgkmcnt(4)
	v_mfma_f32_32x32x16_bf16 v[18:33], v[82:85], v[134:137], v[18:33]
	s_cmpk_lt_u32 s19, 0x100
	s_cselect_b64 s[2:3], -1, 0
	ds_read_b32 v158, v228 offset:31040
	v_add_u32_e32 v159, v230, v139
	s_nop 2
	v_exp_f32_e32 v139, v20
	v_exp_f32_e32 v138, v24
	v_exp_f32_e32 v141, v28
	v_exp_f32_e32 v140, v32
	v_exp_f32_e32 v18, v18
	v_exp_f32_e32 v20, v22
	v_exp_f32_e32 v22, v26
	v_add_f32_e32 v24, 1.0, v138
	v_add_f32_e32 v26, 1.0, v141
	v_add_f32_e32 v19, 1.0, v139
	v_exp_f32_e32 v23, v30
	v_add_f32_e32 v27, 1.0, v140
	v_fmac_f32_e32 v24, v20, v24
	v_fmac_f32_e32 v26, v22, v26
	v_fmac_f32_e32 v19, v18, v19
	v_fmac_f32_e32 v27, v23, v27
	v_rcp_f32_e32 v18, v24
	v_rcp_f32_e32 v22, v27
	v_rcp_f32_e32 v19, v19
	v_rcp_f32_e32 v23, v26
	v_exp_f32_e32 v146, v21
	v_exp_f32_e32 v147, v25
	s_mov_b32 s8, 0xc038aa3b
	s_mov_b32 s4, 0x4038aa3b
	v_mov_b64_e32 v[160:161], s[8:9]
	v_exp_f32_e32 v148, v29
	v_exp_f32_e32 v149, v33
	v_pk_fma_f32 v[20:21], v[138:139], s[4:5], v[160:161] op_sel_hi:[1,0,0]
	s_nop 0
	v_pk_mul_f32 v[214:215], v[20:21], v[18:19]
	v_pk_fma_f32 v[18:19], v[140:141], s[4:5], v[160:161] op_sel_hi:[1,0,0]
	s_nop 0
	v_pk_mul_f32 v[212:213], v[18:19], v[22:23]
	v_add_u32_e32 v231, s7, v229
	ds_read_b128 v[18:21], v231 offset:36928
	ds_read_b128 v[22:25], v231 offset:36944
	ds_read_b128 v[26:29], v231 offset:36960
	ds_read_b128 v[30:33], v231 offset:36976
	s_waitcnt lgkmcnt(5)
	v_mfma_f32_32x32x16_bf16 v[2:17], v[46:49], v[142:145], v[236:251]
	ds_read_b128 v[138:141], v159 offset:16384
	v_add_f32_e32 v162, 1.0, v146
	v_exp_f32_e32 v163, v215
	v_exp_f32_e32 v164, v214
	v_exp_f32_e32 v165, v213
	v_exp_f32_e32 v166, v212
	v_add_f32_e32 v142, 1.0, v147
	v_add_f32_e32 v143, 1.0, v148
	v_add_f32_e32 v144, 1.0, v149
	v_mfma_f32_32x32x16_bf16 v[2:17], v[42:45], v[130:133], v[2:17]
	ds_read_b128 v[146:149], v159 offset:16416
	v_fmac_f32_e32 v162, v162, v163
	v_fmac_f32_e32 v142, v142, v164
	v_fmac_f32_e32 v143, v143, v165
	v_fmac_f32_e32 v144, v144, v166
	v_mfma_f32_32x32x16_bf16 v[2:17], v[38:41], v[154:157], v[2:17]
	ds_read_b128 v[150:153], v159 offset:16448
	v_rcp_f32_e32 v130, v162
	v_rcp_f32_e32 v131, v142
	v_rcp_f32_e32 v132, v143
	v_rcp_f32_e32 v133, v144
	s_waitcnt vmcnt(16)
	v_mfma_f32_32x32x16_bf16 v[2:17], v[34:37], v[134:137], v[2:17]
	ds_read_b128 v[178:181], v159 offset:16480
	v_fma_f32 v130, -v163, v130, v130
	v_fma_f32 v131, -v164, v131, v131
	v_fma_f32 v132, -v165, v132, v132
	v_fma_f32 v133, -v166, v133, v133
	v_add_u32_e32 v211, s6, v210
	v_cvt_pk_bf16_f32 v252, v130, v131
	v_cvt_pk_bf16_f32 v253, v132, v133
	s_nop 3
	v_exp_f32_e32 v131, v4
	v_exp_f32_e32 v130, v8
	v_exp_f32_e32 v133, v12
	v_exp_f32_e32 v132, v16
	v_exp_f32_e32 v2, v2
	v_exp_f32_e32 v4, v6
	v_exp_f32_e32 v6, v10
	v_exp_f32_e32 v7, v14
	v_add_f32_e32 v3, 1.0, v131
	v_add_f32_e32 v8, 1.0, v130
	v_add_f32_e32 v10, 1.0, v133
	v_add_f32_e32 v11, 1.0, v132
	v_fmac_f32_e32 v3, v2, v3
	v_fmac_f32_e32 v8, v4, v8
	v_fmac_f32_e32 v10, v6, v10
	v_fmac_f32_e32 v11, v7, v11
	v_rcp_f32_e32 v3, v3
	v_rcp_f32_e32 v2, v8
	v_rcp_f32_e32 v7, v10
	v_rcp_f32_e32 v6, v11
	v_exp_f32_e32 v134, v5
	v_exp_f32_e32 v135, v9
	v_pk_fma_f32 v[4:5], v[130:131], s[4:5], v[160:161] op_sel_hi:[1,0,0]
	v_exp_f32_e32 v130, v13
	v_pk_mul_f32 v[204:205], v[4:5], v[2:3]
	v_pk_fma_f32 v[2:3], v[132:133], s[4:5], v[160:161] op_sel_hi:[1,0,0]
	v_exp_f32_e32 v131, v17
	v_pk_mul_f32 v[202:203], v[2:3], v[6:7]
	s_waitcnt lgkmcnt(3)
	v_mfma_f32_32x32x16_bf16 v[18:33], v[94:97], v[138:141], v[18:33]
	v_add_f32_e32 v132, 1.0, v134
	v_exp_f32_e32 v133, v205
	v_add_f32_e32 v134, 1.0, v135
	v_exp_f32_e32 v135, v204
	v_exp_f32_e32 v136, v203
	v_exp_f32_e32 v137, v202
	v_add_f32_e32 v130, 1.0, v130
	v_add_f32_e32 v131, 1.0, v131
	s_waitcnt lgkmcnt(2)
	v_mfma_f32_32x32x16_bf16 v[18:33], v[90:93], v[146:149], v[18:33]
	v_fmac_f32_e32 v132, v132, v133
	v_fmac_f32_e32 v134, v134, v135
	v_fmac_f32_e32 v130, v130, v136
	v_fmac_f32_e32 v131, v131, v137
	s_waitcnt lgkmcnt(1)
	v_mfma_f32_32x32x16_bf16 v[18:33], v[86:89], v[150:153], v[18:33]
	v_rcp_f32_e32 v132, v132
	v_rcp_f32_e32 v134, v134
	v_rcp_f32_e32 v130, v130
	v_rcp_f32_e32 v131, v131
	s_waitcnt lgkmcnt(0)
	v_mfma_f32_32x32x16_bf16 v[18:33], v[82:85], v[178:181], v[18:33]
	v_fma_f32 v132, -v133, v132, v132
	v_fma_f32 v133, -v135, v134, v134
	v_fma_f32 v134, -v136, v130, v130
	v_fma_f32 v131, -v137, v131, v131
	v_cvt_pk_bf16_f32 v254, v132, v133
	v_cvt_pk_bf16_f32 v255, v134, v131
	ds_write_b128 v211, v[252:255] offset:0
	s_waitcnt lgkmcnt(0)
	s_barrier
	s_load_dwordx8 s[4:11], s[0:1], 0x10
	ds_read_b32 v194, v228 offset:31168
	ds_read_b128 v[174:177], v210
	v_add_u32_e32 v183, v230, v158
	ds_read_b128 v[170:173], v210 offset:1024
	v_exp_f32_e32 v131, v20
	v_exp_f32_e32 v130, v24
	v_exp_f32_e32 v133, v28
	v_exp_f32_e32 v132, v32
	ds_read_b128 v[166:169], v210 offset:2048
	v_exp_f32_e32 v18, v18
	v_exp_f32_e32 v20, v22
	v_exp_f32_e32 v22, v26
	v_exp_f32_e32 v23, v30
	v_fma_f32 v19, v131, s12, s12
	v_fma_f32 v24, v130, s12, s12
	v_fma_f32 v26, v133, s12, s12
	v_fma_f32 v27, v132, s12, s12
	ds_read_b128 v[162:165], v210 offset:3072
	v_fmac_f32_e32 v19, v18, v19
	v_fmac_f32_e32 v24, v20, v24
	v_fmac_f32_e32 v26, v22, v26
	v_fmac_f32_e32 v27, v23, v27
	ds_read_b128 v[158:161], v210 offset:4096
	v_rcp_f32_e32 v19, v19
	v_rcp_f32_e32 v18, v24
	v_rcp_f32_e32 v23, v26
	v_rcp_f32_e32 v22, v27
	ds_read_b128 v[154:157], v210 offset:5120
	v_exp_f32_e32 v186, v21
	v_exp_f32_e32 v187, v25
	ds_read_b128 v[142:145], v210 offset:6144
	s_mov_b32 s0, 0xc038aa3b
	v_exp_f32_e32 v188, v29
	v_pk_fma_f32 v[200:201], v[130:131], v[18:19], v[18:19] neg_lo:[1,0,0] neg_hi:[1,0,0]
	v_exp_f32_e32 v189, v33
	v_pk_fma_f32 v[198:199], v[132:133], v[22:23], v[22:23] neg_lo:[1,0,0] neg_hi:[1,0,0]
	ds_read_b128 v[130:133], v210 offset:7168
	ds_read_b128 v[18:21], v231 offset:36928
	ds_read_b128 v[22:25], v231 offset:36944
	ds_read_b128 v[26:29], v231 offset:36960
	ds_read_b128 v[30:33], v231 offset:36976
	v_mfma_f32_32x32x16_bf16 v[2:17], v[46:49], v[138:141], v[236:251]
	ds_read_b128 v[134:137], v183 offset:16384
	v_add_f32_e32 v186, 1.0, v186
	v_exp_f32_e32 v190, v201
	v_exp_f32_e32 v191, v200
	v_exp_f32_e32 v192, v199
	v_exp_f32_e32 v193, v198
	v_add_f32_e32 v187, 1.0, v187
	v_add_f32_e32 v188, 1.0, v188
	v_add_f32_e32 v189, 1.0, v189
	v_mfma_f32_32x32x16_bf16 v[2:17], v[42:45], v[146:149], v[2:17]
	ds_read_b128 v[138:141], v183 offset:16416
	v_fmac_f32_e32 v186, v186, v190
	v_fmac_f32_e32 v187, v187, v191
	v_fmac_f32_e32 v188, v188, v192
	v_fmac_f32_e32 v189, v189, v193
	v_mfma_f32_32x32x16_bf16 v[2:17], v[38:41], v[150:153], v[2:17]
	ds_read_b128 v[146:149], v183 offset:16448
	v_rcp_f32_e32 v186, v186
	v_rcp_f32_e32 v187, v187
	v_rcp_f32_e32 v188, v188
	v_rcp_f32_e32 v189, v189
	v_mfma_f32_32x32x16_bf16 v[2:17], v[34:37], v[178:181], v[2:17]
	ds_read_b128 v[150:153], v183 offset:16480
	v_fma_f32 v183, -v190, v186, v186
	v_fma_f32 v186, -v191, v187, v187
	v_fma_f32 v187, -v192, v188, v188
	v_fma_f32 v188, -v193, v189, v189
	s_waitcnt vmcnt(15) lgkmcnt(0)
	v_mfma_f32_32x32x16_bf16 v[18:33], v[126:129], v[174:177], v[18:33]
	v_cvt_pk_bf16_f32 v252, v183, v186
	v_cvt_pk_bf16_f32 v253, v187, v188
	s_waitcnt vmcnt(14)
	v_mfma_f32_32x32x16_bf16 v[18:33], v[122:125], v[170:173], v[18:33]
	s_nop 0
	v_exp_f32_e32 v179, v4
	v_exp_f32_e32 v178, v8
	v_exp_f32_e32 v181, v12
	v_exp_f32_e32 v180, v16
	s_waitcnt vmcnt(13)
	v_mfma_f32_32x32x16_bf16 v[18:33], v[118:121], v[166:169], v[18:33]
	v_exp_f32_e32 v2, v2
	v_exp_f32_e32 v4, v6
	v_exp_f32_e32 v7, v10
	v_exp_f32_e32 v8, v14
	v_fma_f32 v3, v179, s12, s12
	v_fma_f32 v6, v178, s12, s12
	v_fma_f32 v10, v181, s12, s12
	v_fma_f32 v11, v180, s12, s12
	s_waitcnt vmcnt(12)
	v_mfma_f32_32x32x16_bf16 v[18:33], v[114:117], v[162:165], v[18:33]
	v_fmac_f32_e32 v3, v2, v3
	v_fmac_f32_e32 v6, v4, v6
	v_fmac_f32_e32 v10, v7, v10
	v_fmac_f32_e32 v11, v8, v11
	s_waitcnt vmcnt(11)
	v_mfma_f32_32x32x16_bf16 v[18:33], v[110:113], v[158:161], v[18:33]
	v_rcp_f32_e32 v3, v3
	v_rcp_f32_e32 v2, v6
	v_rcp_f32_e32 v7, v10
	v_rcp_f32_e32 v6, v11
	s_waitcnt vmcnt(10)
	v_mfma_f32_32x32x16_bf16 v[18:33], v[106:109], v[154:157], v[18:33]
	v_exp_f32_e32 v183, v5
	v_exp_f32_e32 v186, v9
	s_waitcnt vmcnt(9)
	v_mfma_f32_32x32x16_bf16 v[18:33], v[102:105], v[142:145], v[18:33]
	v_pk_fma_f32 v[206:207], v[178:179], v[2:3], v[2:3] neg_lo:[1,0,0] neg_hi:[1,0,0]
	v_exp_f32_e32 v178, v13
	v_exp_f32_e32 v179, v17
	v_pk_fma_f32 v[208:209], v[180:181], v[6:7], v[6:7] neg_lo:[1,0,0] neg_hi:[1,0,0]
	s_waitcnt vmcnt(8)
	v_mfma_f32_32x32x16_bf16 v[18:33], v[98:101], v[130:133], v[18:33]
	v_mfma_f32_32x32x16_bf16 v[18:33], v[94:97], v[134:137], v[18:33]
	v_add_f32_e32 v180, 1.0, v183
	v_exp_f32_e32 v181, v207
	v_add_f32_e32 v183, 1.0, v186
	v_exp_f32_e32 v184, v206
	v_exp_f32_e32 v185, v209
	v_exp_f32_e32 v186, v208
	v_add_f32_e32 v178, 1.0, v178
	v_add_f32_e32 v179, 1.0, v179
	v_mfma_f32_32x32x16_bf16 v[18:33], v[90:93], v[138:141], v[18:33]
	v_fmac_f32_e32 v180, v180, v181
	v_fmac_f32_e32 v183, v183, v184
	v_fmac_f32_e32 v178, v178, v185
	v_fmac_f32_e32 v179, v179, v186
	v_mfma_f32_32x32x16_bf16 v[18:33], v[86:89], v[146:149], v[18:33]
	v_rcp_f32_e32 v180, v180
	v_rcp_f32_e32 v183, v183
	v_rcp_f32_e32 v178, v178
	v_rcp_f32_e32 v179, v179
	v_mfma_f32_32x32x16_bf16 v[18:33], v[82:85], v[150:153], v[18:33]
	v_fma_f32 v180, -v181, v180, v180
	v_fma_f32 v181, -v184, v183, v183
	v_fma_f32 v183, -v185, v178, v178
	v_fma_f32 v179, -v186, v179, v179
	v_cvt_pk_bf16_f32 v254, v180, v181
	v_cvt_pk_bf16_f32 v255, v183, v179
	ds_write_b128 v211, v[252:255] offset:8192
	s_waitcnt lgkmcnt(0)
	s_barrier
	v_mov_b32_e32 v178, 0x7a40
	v_lshl_add_u32 v232, v182, 2, v178
	s_mov_b32 s1, -1
	s_branch .LBB1_14
.LBB1_13:
	v_mfma_f32_32x32x16_bf16 v[2:17], v[78:81], v[206:209], v[236:251]
	ds_read_b32 v194, v232 offset:384
	ds_read_b128 v[174:177], v210
	v_add_u32_e32 v195, v230, v233
	v_mfma_f32_32x32x16_bf16 v[2:17], v[74:77], v[190:193], v[2:17]
	ds_read_b128 v[170:173], v210 offset:1024
	v_exp_f32_e32 v199, v28
	v_exp_f32_e32 v198, v32
	v_exp_f32_e32 v197, v20
	v_exp_f32_e32 v196, v24
	v_mfma_f32_32x32x16_bf16 v[2:17], v[70:73], v[158:161], v[2:17]
	ds_read_b128 v[166:169], v210 offset:2048
	v_exp_f32_e32 v18, v18
	v_exp_f32_e32 v22, v22
	v_exp_f32_e32 v24, v26
	v_exp_f32_e32 v26, v30
	v_fma_f32 v20, v197, s12, s12
	v_fma_f32 v28, v196, s12, s12
	v_fma_f32 v30, v199, s12, s12
	v_fma_f32 v32, v198, s12, s12
	v_mfma_f32_32x32x16_bf16 v[2:17], v[66:69], v[142:145], v[2:17]
	ds_read_b128 v[162:165], v210 offset:3072
	v_exp_f32_e32 v19, v19
	v_exp_f32_e32 v23, v23
	v_exp_f32_e32 v27, v27
	v_exp_f32_e32 v31, v31
	v_fmac_f32_e32 v20, v18, v20
	v_fmac_f32_e32 v28, v22, v28
	v_fmac_f32_e32 v30, v24, v30
	v_fmac_f32_e32 v32, v26, v32
	v_mfma_f32_32x32x16_bf16 v[2:17], v[62:65], v[154:157], v[2:17]
	ds_read_b128 v[158:161], v210 offset:4096
	v_add_f32_e32 v22, 1.0, v19
	v_rcp_f32_e32 v19, v20
	v_rcp_f32_e32 v18, v28
	v_add_f32_e32 v20, 1.0, v23
	v_rcp_f32_e32 v191, v30
	v_rcp_f32_e32 v190, v32
	v_mfma_f32_32x32x16_bf16 v[2:17], v[58:61], v[182:185], v[2:17]
	ds_read_b128 v[154:157], v210 offset:5120
	v_exp_f32_e32 v206, v21
	v_exp_f32_e32 v207, v25
	v_add_f32_e32 v23, 1.0, v27
	v_rcp_f32_e32 v192, v20
	v_add_f32_e32 v20, 1.0, v31
	v_rcp_f32_e32 v193, v22
	v_mfma_f32_32x32x16_bf16 v[2:17], v[54:57], v[186:189], v[2:17]
	ds_read_b128 v[142:145], v210 offset:6144
	v_exp_f32_e32 v208, v29
	v_exp_f32_e32 v209, v33
	v_rcp_f32_e32 v183, v23
	v_rcp_f32_e32 v182, v20
	v_mfma_f32_32x32x16_bf16 v[2:17], v[50:53], v[134:137], v[2:17]
	ds_read_b128 v[130:133], v210 offset:7168
	v_fma_f32 v186, -v196, v18, v18
	v_fma_f32 v187, -v197, v19, v19
	ds_read_b128 v[18:21], v231 offset:36928
	ds_read_b128 v[22:25], v231 offset:36944
	ds_read_b128 v[26:29], v231 offset:36960
	ds_read_b128 v[30:33], v231 offset:36976
	v_pk_fma_f32 v[200:201], v[192:193], v[220:221], v[186:187]
	v_pk_fma_f32 v[134:135], v[198:199], v[190:191], v[190:191] neg_lo:[1,0,0] neg_hi:[1,0,0]
	s_nop 0
	v_pk_fma_f32 v[198:199], v[182:183], v[222:223], v[134:135]
	v_mfma_f32_32x32x16_bf16 v[2:17], v[46:49], v[138:141], v[2:17]
	ds_read_b128 v[134:137], v195 offset:16384
	v_add_f32_e32 v182, 1.0, v206
	v_exp_f32_e32 v183, v201
	v_exp_f32_e32 v186, v200
	v_exp_f32_e32 v187, v199
	v_exp_f32_e32 v188, v198
	v_add_f32_e32 v189, 1.0, v207
	v_add_f32_e32 v190, 1.0, v208
	v_add_f32_e32 v191, 1.0, v209
	v_mfma_f32_32x32x16_bf16 v[2:17], v[42:45], v[146:149], v[2:17]
	ds_read_b128 v[138:141], v195 offset:16416
	v_fmac_f32_e32 v182, v182, v183
	v_fmac_f32_e32 v189, v189, v186
	v_fmac_f32_e32 v190, v190, v187
	v_fmac_f32_e32 v191, v191, v188
	v_mfma_f32_32x32x16_bf16 v[2:17], v[38:41], v[150:153], v[2:17]
	ds_read_b128 v[146:149], v195 offset:16448
	v_rcp_f32_e32 v182, v182
	v_rcp_f32_e32 v189, v189
	v_rcp_f32_e32 v190, v190
	v_rcp_f32_e32 v191, v191
	v_mfma_f32_32x32x16_bf16 v[2:17], v[34:37], v[178:181], v[2:17]
	ds_read_b128 v[150:153], v195 offset:16480
	v_fma_f32 v182, -v183, v182, v182
	v_fma_f32 v183, -v186, v189, v189
	v_fma_f32 v186, -v187, v190, v190
	v_fma_f32 v187, -v188, v191, v191
	s_waitcnt lgkmcnt(4)
	v_mfma_f32_32x32x16_bf16 v[18:33], v[126:129], v[174:177], v[18:33]
	v_cvt_pk_bf16_f32 v252, v182, v183
	v_cvt_pk_bf16_f32 v253, v186, v187
	v_mfma_f32_32x32x16_bf16 v[18:33], v[122:125], v[170:173], v[18:33]
	s_nop 1
	v_exp_f32_e32 v179, v4
	v_exp_f32_e32 v178, v8
	v_exp_f32_e32 v181, v12
	v_exp_f32_e32 v180, v16
	v_mfma_f32_32x32x16_bf16 v[18:33], v[118:121], v[166:169], v[18:33]
	v_exp_f32_e32 v2, v2
	v_exp_f32_e32 v6, v6
	v_exp_f32_e32 v10, v10
	v_exp_f32_e32 v12, v14
	v_fma_f32 v4, v179, s12, s12
	v_fma_f32 v8, v178, s12, s12
	v_fma_f32 v14, v181, s12, s12
	v_fma_f32 v16, v180, s12, s12
	v_mfma_f32_32x32x16_bf16 v[18:33], v[114:117], v[162:165], v[18:33]
	v_exp_f32_e32 v3, v3
	v_fmac_f32_e32 v4, v2, v4
	v_exp_f32_e32 v2, v7
	v_fmac_f32_e32 v8, v6, v8
	v_exp_f32_e32 v6, v11
	v_exp_f32_e32 v7, v15
	v_fmac_f32_e32 v14, v10, v14
	v_fmac_f32_e32 v16, v12, v16
	v_mfma_f32_32x32x16_bf16 v[18:33], v[110:113], v[158:161], v[18:33]
	v_add_f32_e32 v10, 1.0, v3
	v_rcp_f32_e32 v3, v4
	v_add_f32_e32 v4, 1.0, v2
	v_rcp_f32_e32 v2, v8
	v_rcp_f32_e32 v183, v14
	v_rcp_f32_e32 v182, v16
	v_mfma_f32_32x32x16_bf16 v[18:33], v[106:109], v[154:157], v[18:33]
	v_add_f32_e32 v6, 1.0, v6
	v_add_f32_e32 v7, 1.0, v7
	v_rcp_f32_e32 v187, v10
	v_rcp_f32_e32 v186, v4
	v_exp_f32_e32 v190, v5
	v_exp_f32_e32 v191, v9
	v_mfma_f32_32x32x16_bf16 v[18:33], v[102:105], v[142:145], v[18:33]
	v_rcp_f32_e32 v189, v6
	v_rcp_f32_e32 v188, v7
	v_exp_f32_e32 v192, v13
	v_exp_f32_e32 v193, v17
	v_mfma_f32_32x32x16_bf16 v[18:33], v[98:101], v[130:133], v[18:33]
	v_fma_f32 v178, -v178, v2, v2
	v_fma_f32 v179, -v179, v3, v3
	v_pk_fma_f32 v[206:207], v[186:187], v[216:217], v[178:179]
	s_nop 0
	v_pk_fma_f32 v[178:179], v[180:181], v[182:183], v[182:183] neg_lo:[1,0,0] neg_hi:[1,0,0]
	s_nop 0
	v_pk_fma_f32 v[208:209], v[188:189], v[218:219], v[178:179]
	s_waitcnt lgkmcnt(3)
	v_mfma_f32_32x32x16_bf16 v[18:33], v[94:97], v[134:137], v[18:33]
	v_add_f32_e32 v178, 1.0, v190
	v_exp_f32_e32 v179, v207
	v_add_f32_e32 v180, 1.0, v191
	v_exp_f32_e32 v181, v206
	v_exp_f32_e32 v182, v209
	v_exp_f32_e32 v183, v208
	v_add_f32_e32 v184, 1.0, v192
	v_add_f32_e32 v185, 1.0, v193
	s_waitcnt lgkmcnt(2)
	v_mfma_f32_32x32x16_bf16 v[18:33], v[90:93], v[138:141], v[18:33]
	v_fmac_f32_e32 v178, v178, v179
	v_fmac_f32_e32 v180, v180, v181
	v_fmac_f32_e32 v184, v184, v182
	v_fmac_f32_e32 v185, v185, v183
	s_waitcnt lgkmcnt(1)
	v_mfma_f32_32x32x16_bf16 v[18:33], v[86:89], v[146:149], v[18:33]
	v_rcp_f32_e32 v178, v178
	v_rcp_f32_e32 v180, v180
	v_rcp_f32_e32 v184, v184
	v_rcp_f32_e32 v185, v185
	s_waitcnt lgkmcnt(0)
	v_mfma_f32_32x32x16_bf16 v[18:33], v[82:85], v[150:153], v[18:33]
	v_fma_f32 v178, -v179, v178, v178
	v_fma_f32 v179, -v181, v180, v180
	v_fma_f32 v180, -v182, v184, v184
	v_fma_f32 v181, -v183, v185, v185
	v_cvt_pk_bf16_f32 v254, v178, v179
	v_cvt_pk_bf16_f32 v255, v180, v181
	ds_write_b128 v211, v[252:255] offset:8192
	s_waitcnt lgkmcnt(0)
	s_barrier
	s_add_i32 s1, s1, 2
	s_cmp_gt_u32 s1, 16
	v_add_u32_e32 v232, 0x200, v232
	s_cbranch_scc1 .LBB1_30
.LBB1_14:
	s_waitcnt vmcnt(7)
	v_mfma_f32_32x32x16_bf16 v[2:17], v[78:81], v[174:177], v[236:251]
	v_add_u32_e32 v192, v230, v194
	ds_read_b32 v216, v232
	ds_read_b128 v[194:197], v210 offset:8192
	s_waitcnt vmcnt(6)
	v_mfma_f32_32x32x16_bf16 v[2:17], v[74:77], v[170:173], v[2:17]
	ds_read_b128 v[178:181], v210 offset:9216
	v_exp_f32_e32 v187, v20
	v_exp_f32_e32 v186, v24
	v_exp_f32_e32 v189, v28
	v_exp_f32_e32 v188, v32
	s_waitcnt vmcnt(5)
	v_mfma_f32_32x32x16_bf16 v[2:17], v[70:73], v[166:169], v[2:17]
	ds_read_b128 v[170:173], v210 offset:10240
	v_exp_f32_e32 v18, v18
	v_exp_f32_e32 v22, v22
	v_exp_f32_e32 v24, v26
	v_exp_f32_e32 v26, v30
	v_fma_f32 v20, v187, s12, s12
	v_fma_f32 v28, v186, s12, s12
	v_fma_f32 v30, v189, s12, s12
	v_fma_f32 v32, v188, s12, s12
	s_waitcnt vmcnt(4)
	v_mfma_f32_32x32x16_bf16 v[2:17], v[66:69], v[162:165], v[2:17]
	ds_read_b128 v[166:169], v210 offset:11264
	v_exp_f32_e32 v19, v19
	v_exp_f32_e32 v23, v23
	v_exp_f32_e32 v27, v27
	v_exp_f32_e32 v31, v31
	v_fmac_f32_e32 v20, v18, v20
	v_fmac_f32_e32 v28, v22, v28
	v_fmac_f32_e32 v30, v24, v30
	v_fmac_f32_e32 v32, v26, v32
	s_waitcnt vmcnt(3)
	v_mfma_f32_32x32x16_bf16 v[2:17], v[62:65], v[158:161], v[2:17]
	ds_read_b128 v[162:165], v210 offset:12288
	v_add_f32_e32 v22, 1.0, v19
	v_rcp_f32_e32 v19, v20
	v_rcp_f32_e32 v18, v28
	v_rcp_f32_e32 v191, v30
	v_rcp_f32_e32 v190, v32
	v_add_f32_e32 v20, 1.0, v23
	s_waitcnt vmcnt(2)
	v_mfma_f32_32x32x16_bf16 v[2:17], v[58:61], v[154:157], v[2:17]
	ds_read_b128 v[174:177], v210 offset:13312
	v_rcp_f32_e32 v159, v22
	v_rcp_f32_e32 v158, v20
	v_exp_f32_e32 v160, v21
	v_exp_f32_e32 v161, v25
	v_add_f32_e32 v23, 1.0, v27
	v_add_f32_e32 v20, 1.0, v31
	s_waitcnt vmcnt(1)
	v_mfma_f32_32x32x16_bf16 v[2:17], v[54:57], v[142:145], v[2:17]
	ds_read_b128 v[182:185], v210 offset:14336
	v_rcp_f32_e32 v155, v23
	v_rcp_f32_e32 v154, v20
	v_exp_f32_e32 v193, v29
	v_exp_f32_e32 v217, v33
	s_waitcnt vmcnt(0)
	v_mfma_f32_32x32x16_bf16 v[2:17], v[50:53], v[130:133], v[2:17]
	ds_read_b128 v[142:145], v210 offset:15360
	v_fma_f32 v156, -v186, v18, v18
	v_fma_f32 v157, -v187, v19, v19
	ds_read_b128 v[18:21], v231 offset:36928
	ds_read_b128 v[22:25], v231 offset:36944
	ds_read_b128 v[26:29], v231 offset:36960
	ds_read_b128 v[30:33], v231 offset:36976
	v_pk_fma_f32 v[214:215], v[158:159], v[214:215], v[156:157]
	v_pk_fma_f32 v[130:131], v[188:189], v[190:191], v[190:191] neg_lo:[1,0,0] neg_hi:[1,0,0]
	s_nop 0
	v_pk_fma_f32 v[212:213], v[154:155], v[212:213], v[130:131]
	v_mfma_f32_32x32x16_bf16 v[2:17], v[46:49], v[134:137], v[2:17]
	ds_read_b128 v[154:157], v192 offset:16384
	v_add_f32_e32 v130, 1.0, v160
	v_exp_f32_e32 v131, v215
	v_exp_f32_e32 v132, v214
	v_exp_f32_e32 v133, v213
	v_exp_f32_e32 v220, v212
	v_add_f32_e32 v134, 1.0, v161
	v_add_f32_e32 v135, 1.0, v193
	v_add_f32_e32 v136, 1.0, v217
	v_mfma_f32_32x32x16_bf16 v[2:17], v[42:45], v[138:141], v[2:17]
	ds_read_b128 v[158:161], v192 offset:16416
	v_fmac_f32_e32 v130, v130, v131
	v_fmac_f32_e32 v134, v134, v132
	v_fmac_f32_e32 v135, v135, v133
	v_fmac_f32_e32 v136, v136, v220
	v_mfma_f32_32x32x16_bf16 v[2:17], v[38:41], v[146:149], v[2:17]
	ds_read_b128 v[186:189], v192 offset:16448
	v_rcp_f32_e32 v130, v130
	v_rcp_f32_e32 v134, v134
	v_rcp_f32_e32 v135, v135
	v_rcp_f32_e32 v136, v136
	v_mfma_f32_32x32x16_bf16 v[2:17], v[34:37], v[150:153], v[2:17]
	ds_read_b128 v[190:193], v192 offset:16480
	v_fma_f32 v130, -v131, v130, v130
	v_fma_f32 v131, -v132, v134, v134
	v_fma_f32 v132, -v133, v135, v135
	v_fma_f32 v133, -v220, v136, v136
	s_waitcnt lgkmcnt(4)
	v_mfma_f32_32x32x16_bf16 v[18:33], v[126:129], v[194:197], v[18:33]
	v_cvt_pk_bf16_f32 v252, v130, v131
	v_cvt_pk_bf16_f32 v253, v132, v133
	v_mfma_f32_32x32x16_bf16 v[18:33], v[122:125], v[178:181], v[18:33]
	s_nop 1
	v_exp_f32_e32 v131, v4
	v_exp_f32_e32 v130, v8
	v_exp_f32_e32 v133, v12
	v_exp_f32_e32 v132, v16
	v_mfma_f32_32x32x16_bf16 v[18:33], v[118:121], v[170:173], v[18:33]
	v_exp_f32_e32 v2, v2
	v_exp_f32_e32 v6, v6
	v_exp_f32_e32 v10, v10
	v_exp_f32_e32 v12, v14
	v_fma_f32 v4, v131, s12, s12
	v_fma_f32 v8, v130, s12, s12
	v_fma_f32 v14, v133, s12, s12
	v_fma_f32 v16, v132, s12, s12
	v_mfma_f32_32x32x16_bf16 v[18:33], v[114:117], v[166:169], v[18:33]
	v_exp_f32_e32 v3, v3
	v_fmac_f32_e32 v4, v2, v4
	v_exp_f32_e32 v2, v7
	v_fmac_f32_e32 v8, v6, v8
	v_exp_f32_e32 v6, v11
	v_exp_f32_e32 v7, v15
	v_fmac_f32_e32 v14, v10, v14
	v_fmac_f32_e32 v16, v12, v16
	v_mfma_f32_32x32x16_bf16 v[18:33], v[110:113], v[162:165], v[18:33]
	v_add_f32_e32 v10, 1.0, v3
	v_rcp_f32_e32 v3, v4
	v_add_f32_e32 v4, 1.0, v2
	v_rcp_f32_e32 v2, v8
	v_rcp_f32_e32 v135, v14
	v_rcp_f32_e32 v134, v16
	v_mfma_f32_32x32x16_bf16 v[18:33], v[106:109], v[174:177], v[18:33]
	v_add_f32_e32 v6, 1.0, v6
	v_add_f32_e32 v7, 1.0, v7
	v_rcp_f32_e32 v137, v10
	v_rcp_f32_e32 v136, v4
	v_exp_f32_e32 v140, v5
	v_exp_f32_e32 v141, v9
	v_mfma_f32_32x32x16_bf16 v[18:33], v[102:105], v[182:185], v[18:33]
	v_rcp_f32_e32 v139, v6
	v_rcp_f32_e32 v138, v7
	v_exp_f32_e32 v146, v13
	v_exp_f32_e32 v147, v17
	v_mfma_f32_32x32x16_bf16 v[18:33], v[98:101], v[142:145], v[18:33]
	v_fma_f32 v130, -v130, v2, v2
	v_fma_f32 v131, -v131, v3, v3
	v_pk_fma_f32 v[224:225], v[136:137], v[204:205], v[130:131]
	s_nop 0
	v_pk_fma_f32 v[130:131], v[132:133], v[134:135], v[134:135] neg_lo:[1,0,0] neg_hi:[1,0,0]
	s_nop 0
	v_pk_fma_f32 v[226:227], v[138:139], v[202:203], v[130:131]
	s_waitcnt lgkmcnt(3)
	v_mfma_f32_32x32x16_bf16 v[18:33], v[94:97], v[154:157], v[18:33]
	v_add_f32_e32 v130, 1.0, v140
	v_exp_f32_e32 v131, v225
	v_add_f32_e32 v132, 1.0, v141
	v_exp_f32_e32 v133, v224
	v_exp_f32_e32 v134, v227
	v_exp_f32_e32 v135, v226
	v_add_f32_e32 v136, 1.0, v146
	v_add_f32_e32 v137, 1.0, v147
	s_waitcnt lgkmcnt(2)
	v_mfma_f32_32x32x16_bf16 v[18:33], v[90:93], v[158:161], v[18:33]
	v_fmac_f32_e32 v130, v130, v131
	v_fmac_f32_e32 v132, v132, v133
	v_fmac_f32_e32 v136, v136, v134
	v_fmac_f32_e32 v137, v137, v135
	s_waitcnt lgkmcnt(1)
	v_mfma_f32_32x32x16_bf16 v[18:33], v[86:89], v[186:189], v[18:33]
	v_rcp_f32_e32 v130, v130
	v_rcp_f32_e32 v132, v132
	v_rcp_f32_e32 v136, v136
	v_rcp_f32_e32 v137, v137
	s_waitcnt lgkmcnt(0)
	v_mfma_f32_32x32x16_bf16 v[18:33], v[82:85], v[190:193], v[18:33]
	v_fma_f32 v130, -v131, v130, v130
	v_fma_f32 v131, -v133, v132, v132
	v_fma_f32 v132, -v134, v136, v136
	v_fma_f32 v133, -v135, v137, v137
	v_cvt_pk_bf16_f32 v254, v130, v131
	v_cvt_pk_bf16_f32 v255, v132, v133
	ds_write_b128 v211, v[252:255] offset:0
	s_waitcnt lgkmcnt(0)
	s_barrier
	v_mfma_f32_32x32x16_bf16 v[2:17], v[78:81], v[194:197], v[236:251]
	ds_read_b32 v233, v232 offset:128
	ds_read_b128 v[202:205], v210
	v_add_u32_e32 v216, v230, v216
	v_mfma_f32_32x32x16_bf16 v[2:17], v[74:77], v[178:181], v[2:17]
	ds_read_b128 v[194:197], v210 offset:1024
	v_exp_f32_e32 v147, v20
	v_exp_f32_e32 v146, v24
	v_exp_f32_e32 v149, v28
	v_exp_f32_e32 v148, v32
	v_mfma_f32_32x32x16_bf16 v[2:17], v[70:73], v[170:173], v[2:17]
	ds_read_b128 v[138:141], v210 offset:2048
	v_exp_f32_e32 v18, v18
	v_exp_f32_e32 v22, v22
	v_exp_f32_e32 v24, v26
	v_exp_f32_e32 v26, v30
	v_fma_f32 v20, v147, s12, s12
	v_fma_f32 v28, v146, s12, s12
	v_fma_f32 v30, v149, s12, s12
	v_fma_f32 v32, v148, s12, s12
	v_mfma_f32_32x32x16_bf16 v[2:17], v[66:69], v[166:169], v[2:17]
	ds_read_b128 v[134:137], v210 offset:3072
	v_exp_f32_e32 v19, v19
	v_exp_f32_e32 v23, v23
	v_exp_f32_e32 v27, v27
	v_exp_f32_e32 v31, v31
	v_fmac_f32_e32 v20, v18, v20
	v_fmac_f32_e32 v28, v22, v28
	v_fmac_f32_e32 v30, v24, v30
	v_fmac_f32_e32 v32, v26, v32
	v_mfma_f32_32x32x16_bf16 v[2:17], v[62:65], v[162:165], v[2:17]
	ds_read_b128 v[166:169], v210 offset:4096
	v_add_f32_e32 v22, 1.0, v19
	v_rcp_f32_e32 v19, v20
	v_rcp_f32_e32 v18, v28
	v_rcp_f32_e32 v151, v30
	v_rcp_f32_e32 v150, v32
	v_add_f32_e32 v20, 1.0, v23
	v_mfma_f32_32x32x16_bf16 v[2:17], v[58:61], v[174:177], v[2:17]
	ds_read_b128 v[162:165], v210 offset:5120
	v_rcp_f32_e32 v153, v22
	v_rcp_f32_e32 v152, v20
	v_add_f32_e32 v23, 1.0, v27
	v_add_f32_e32 v20, 1.0, v31
	v_exp_f32_e32 v180, v21
	v_exp_f32_e32 v181, v25
	v_mfma_f32_32x32x16_bf16 v[2:17], v[54:57], v[182:185], v[2:17]
	ds_read_b128 v[170:173], v210 offset:6144
	v_rcp_f32_e32 v175, v23
	v_rcp_f32_e32 v174, v20
	v_exp_f32_e32 v176, v29
	v_exp_f32_e32 v177, v33
	v_mfma_f32_32x32x16_bf16 v[2:17], v[50:53], v[142:145], v[2:17]
	ds_read_b128 v[130:133], v210 offset:7168
	v_fma_f32 v146, -v146, v18, v18
	v_fma_f32 v147, -v147, v19, v19
	ds_read_b128 v[18:21], v231 offset:36928
	ds_read_b128 v[22:25], v231 offset:36944
	ds_read_b128 v[26:29], v231 offset:36960
	ds_read_b128 v[30:33], v231 offset:36976
	v_pk_fma_f32 v[220:221], v[152:153], v[200:201], v[146:147]
	v_pk_fma_f32 v[142:143], v[148:149], v[150:151], v[150:151] neg_lo:[1,0,0] neg_hi:[1,0,0]
	s_nop 0
	v_pk_fma_f32 v[222:223], v[174:175], v[198:199], v[142:143]
	v_mfma_f32_32x32x16_bf16 v[2:17], v[46:49], v[154:157], v[2:17]
	ds_read_b128 v[146:149], v216 offset:16384
	v_add_f32_e32 v142, 1.0, v180
	v_exp_f32_e32 v143, v221
	v_exp_f32_e32 v144, v220
	v_exp_f32_e32 v145, v223
	v_exp_f32_e32 v180, v222
	v_add_f32_e32 v154, 1.0, v181
	v_add_f32_e32 v155, 1.0, v176
	v_add_f32_e32 v156, 1.0, v177
	v_mfma_f32_32x32x16_bf16 v[2:17], v[42:45], v[158:161], v[2:17]
	ds_read_b128 v[150:153], v216 offset:16416
	v_fmac_f32_e32 v142, v142, v143
	v_fmac_f32_e32 v154, v154, v144
	v_fmac_f32_e32 v155, v155, v145
	v_fmac_f32_e32 v156, v156, v180
	v_mfma_f32_32x32x16_bf16 v[2:17], v[38:41], v[186:189], v[2:17]
	ds_read_b128 v[174:177], v216 offset:16448
	v_rcp_f32_e32 v142, v142
	v_rcp_f32_e32 v154, v154
	v_rcp_f32_e32 v155, v155
	v_rcp_f32_e32 v156, v156
	v_mfma_f32_32x32x16_bf16 v[2:17], v[34:37], v[190:193], v[2:17]
	ds_read_b128 v[198:201], v216 offset:16480
	v_fma_f32 v142, -v143, v142, v142
	v_fma_f32 v143, -v144, v154, v154
	v_fma_f32 v144, -v145, v155, v155
	v_fma_f32 v145, -v180, v156, v156
	s_waitcnt lgkmcnt(4)
	v_mfma_f32_32x32x16_bf16 v[18:33], v[126:129], v[202:205], v[18:33]
	v_cvt_pk_bf16_f32 v252, v142, v143
	v_cvt_pk_bf16_f32 v253, v144, v145
	v_mfma_f32_32x32x16_bf16 v[18:33], v[122:125], v[194:197], v[18:33]
	s_nop 1
	v_exp_f32_e32 v143, v4
	v_exp_f32_e32 v142, v8
	v_exp_f32_e32 v145, v12
	v_exp_f32_e32 v144, v16
	v_mfma_f32_32x32x16_bf16 v[18:33], v[118:121], v[138:141], v[18:33]
	v_exp_f32_e32 v2, v2
	v_exp_f32_e32 v6, v6
	v_exp_f32_e32 v10, v10
	v_exp_f32_e32 v12, v14
	v_fma_f32 v4, v143, s12, s12
	v_fma_f32 v8, v142, s12, s12
	v_fma_f32 v14, v145, s12, s12
	v_fma_f32 v16, v144, s12, s12
	v_mfma_f32_32x32x16_bf16 v[18:33], v[114:117], v[134:137], v[18:33]
	v_exp_f32_e32 v3, v3
	v_fmac_f32_e32 v4, v2, v4
	v_exp_f32_e32 v2, v7
	v_fmac_f32_e32 v8, v6, v8
	v_exp_f32_e32 v6, v11
	v_exp_f32_e32 v7, v15
	v_fmac_f32_e32 v14, v10, v14
	v_fmac_f32_e32 v16, v12, v16
	v_mfma_f32_32x32x16_bf16 v[18:33], v[110:113], v[166:169], v[18:33]
	v_add_f32_e32 v10, 1.0, v3
	v_rcp_f32_e32 v3, v4
	v_add_f32_e32 v4, 1.0, v2
	v_rcp_f32_e32 v2, v8
	v_rcp_f32_e32 v155, v14
	v_rcp_f32_e32 v154, v16
	v_mfma_f32_32x32x16_bf16 v[18:33], v[106:109], v[162:165], v[18:33]
	v_add_f32_e32 v6, 1.0, v6
	v_add_f32_e32 v7, 1.0, v7
	v_rcp_f32_e32 v157, v10
	v_rcp_f32_e32 v156, v4
	v_exp_f32_e32 v160, v5
	v_exp_f32_e32 v161, v9
	v_mfma_f32_32x32x16_bf16 v[18:33], v[102:105], v[170:173], v[18:33]
	v_rcp_f32_e32 v159, v6
	v_rcp_f32_e32 v158, v7
	v_exp_f32_e32 v180, v13
	v_exp_f32_e32 v181, v17
	v_mfma_f32_32x32x16_bf16 v[18:33], v[98:101], v[130:133], v[18:33]
	v_fma_f32 v142, -v142, v2, v2
	v_fma_f32 v143, -v143, v3, v3
	v_pk_fma_f32 v[216:217], v[156:157], v[206:207], v[142:143]
	s_nop 0
	v_pk_fma_f32 v[142:143], v[144:145], v[154:155], v[154:155] neg_lo:[1,0,0] neg_hi:[1,0,0]
	s_nop 0
	v_pk_fma_f32 v[218:219], v[158:159], v[208:209], v[142:143]
	s_waitcnt lgkmcnt(3)
	v_mfma_f32_32x32x16_bf16 v[18:33], v[94:97], v[146:149], v[18:33]
	v_add_f32_e32 v142, 1.0, v160
	v_exp_f32_e32 v143, v217
	v_add_f32_e32 v144, 1.0, v161
	v_exp_f32_e32 v145, v216
	v_exp_f32_e32 v154, v219
	v_exp_f32_e32 v155, v218
	v_add_f32_e32 v156, 1.0, v180
	v_add_f32_e32 v157, 1.0, v181
	s_waitcnt lgkmcnt(2)
	v_mfma_f32_32x32x16_bf16 v[18:33], v[90:93], v[150:153], v[18:33]
	v_fmac_f32_e32 v142, v142, v143
	v_fmac_f32_e32 v144, v144, v145
	v_fmac_f32_e32 v156, v156, v154
	v_fmac_f32_e32 v157, v157, v155
	s_waitcnt lgkmcnt(1)
	v_mfma_f32_32x32x16_bf16 v[18:33], v[86:89], v[174:177], v[18:33]
	v_rcp_f32_e32 v142, v142
	v_rcp_f32_e32 v144, v144
	v_rcp_f32_e32 v156, v156
	v_rcp_f32_e32 v157, v157
	s_waitcnt lgkmcnt(0)
	v_mfma_f32_32x32x16_bf16 v[18:33], v[82:85], v[198:201], v[18:33]
	v_fma_f32 v142, -v143, v142, v142
	v_fma_f32 v143, -v145, v144, v144
	v_fma_f32 v144, -v154, v156, v156
	v_fma_f32 v145, -v155, v157, v157
	v_cvt_pk_bf16_f32 v254, v142, v143
	v_cvt_pk_bf16_f32 v255, v144, v145
	ds_write_b128 v211, v[252:255] offset:8192
	s_waitcnt lgkmcnt(0)
	s_barrier
	v_mfma_f32_32x32x16_bf16 v[2:17], v[78:81], v[202:205], v[236:251]
	v_add_u32_e32 v234, v230, v233
	ds_read_b32 v233, v232 offset:256
	ds_read_b128 v[206:209], v210 offset:8192
	v_mfma_f32_32x32x16_bf16 v[2:17], v[74:77], v[194:197], v[2:17]
	ds_read_b128 v[190:193], v210 offset:9216
	v_exp_f32_e32 v179, v20
	v_exp_f32_e32 v178, v24
	v_exp_f32_e32 v181, v28
	v_exp_f32_e32 v180, v32
	v_mfma_f32_32x32x16_bf16 v[2:17], v[70:73], v[138:141], v[2:17]
	ds_read_b128 v[158:161], v210 offset:10240
	v_exp_f32_e32 v18, v18
	v_exp_f32_e32 v22, v22
	v_exp_f32_e32 v24, v26
	v_exp_f32_e32 v26, v30
	v_fma_f32 v20, v179, s12, s12
	v_fma_f32 v28, v178, s12, s12
	v_fma_f32 v30, v181, s12, s12
	v_fma_f32 v32, v180, s12, s12
	v_mfma_f32_32x32x16_bf16 v[2:17], v[66:69], v[134:137], v[2:17]
	ds_read_b128 v[142:145], v210 offset:11264
	v_exp_f32_e32 v19, v19
	v_exp_f32_e32 v23, v23
	v_exp_f32_e32 v27, v27
	v_exp_f32_e32 v31, v31
	v_fmac_f32_e32 v20, v18, v20
	v_fmac_f32_e32 v28, v22, v28
	v_fmac_f32_e32 v30, v24, v30
	v_fmac_f32_e32 v32, v26, v32
	v_mfma_f32_32x32x16_bf16 v[2:17], v[62:65], v[166:169], v[2:17]
	ds_read_b128 v[154:157], v210 offset:12288
	v_add_f32_e32 v22, 1.0, v19
	v_rcp_f32_e32 v19, v20
	v_rcp_f32_e32 v18, v28
	v_rcp_f32_e32 v139, v30
	v_rcp_f32_e32 v138, v32
	v_add_f32_e32 v20, 1.0, v23
	v_mfma_f32_32x32x16_bf16 v[2:17], v[58:61], v[162:165], v[2:17]
	ds_read_b128 v[182:185], v210 offset:13312
	v_rcp_f32_e32 v141, v22
	v_rcp_f32_e32 v140, v20
	v_add_f32_e32 v23, 1.0, v27
	v_add_f32_e32 v20, 1.0, v31
	v_exp_f32_e32 v168, v21
	v_exp_f32_e32 v169, v25
	v_mfma_f32_32x32x16_bf16 v[2:17], v[54:57], v[170:173], v[2:17]
	ds_read_b128 v[186:189], v210 offset:14336
	v_rcp_f32_e32 v163, v23
	v_rcp_f32_e32 v162, v20
	v_exp_f32_e32 v194, v29
	v_exp_f32_e32 v195, v33
	v_mfma_f32_32x32x16_bf16 v[2:17], v[50:53], v[130:133], v[2:17]
	ds_read_b128 v[134:137], v210 offset:15360
	v_fma_f32 v166, -v178, v18, v18
	v_fma_f32 v167, -v179, v19, v19
	ds_read_b128 v[18:21], v231 offset:36928
	ds_read_b128 v[22:25], v231 offset:36944
	ds_read_b128 v[26:29], v231 offset:36960
	ds_read_b128 v[30:33], v231 offset:36976
	v_pk_fma_f32 v[214:215], v[140:141], v[214:215], v[166:167]
	v_pk_fma_f32 v[130:131], v[180:181], v[138:139], v[138:139] neg_lo:[1,0,0] neg_hi:[1,0,0]
	s_nop 0
	v_pk_fma_f32 v[212:213], v[162:163], v[212:213], v[130:131]
	v_mfma_f32_32x32x16_bf16 v[2:17], v[46:49], v[146:149], v[2:17]
	ds_read_b128 v[138:141], v234 offset:16384
	v_add_f32_e32 v130, 1.0, v168
	v_exp_f32_e32 v131, v215
	v_exp_f32_e32 v132, v214
	v_exp_f32_e32 v133, v213
	v_exp_f32_e32 v162, v212
	v_add_f32_e32 v163, 1.0, v169
	v_add_f32_e32 v166, 1.0, v194
	v_add_f32_e32 v167, 1.0, v195
	v_mfma_f32_32x32x16_bf16 v[2:17], v[42:45], v[150:153], v[2:17]
	ds_read_b128 v[146:149], v234 offset:16416
	v_fmac_f32_e32 v130, v130, v131
	v_fmac_f32_e32 v163, v163, v132
	v_fmac_f32_e32 v166, v166, v133
	v_fmac_f32_e32 v167, v167, v162
	v_mfma_f32_32x32x16_bf16 v[2:17], v[38:41], v[174:177], v[2:17]
	ds_read_b128 v[150:153], v234 offset:16448
	v_rcp_f32_e32 v130, v130
	v_rcp_f32_e32 v163, v163
	v_rcp_f32_e32 v166, v166
	v_rcp_f32_e32 v167, v167
	v_mfma_f32_32x32x16_bf16 v[2:17], v[34:37], v[198:201], v[2:17]
	ds_read_b128 v[178:181], v234 offset:16480
	v_fma_f32 v130, -v131, v130, v130
	v_fma_f32 v131, -v132, v163, v163
	v_fma_f32 v132, -v133, v166, v166
	v_fma_f32 v133, -v162, v167, v167
	s_waitcnt lgkmcnt(4)
	v_mfma_f32_32x32x16_bf16 v[18:33], v[126:129], v[206:209], v[18:33]
	v_cvt_pk_bf16_f32 v252, v130, v131
	v_cvt_pk_bf16_f32 v253, v132, v133
	v_mfma_f32_32x32x16_bf16 v[18:33], v[122:125], v[190:193], v[18:33]
	s_nop 1
	v_exp_f32_e32 v131, v4
	v_exp_f32_e32 v130, v8
	v_exp_f32_e32 v133, v12
	v_exp_f32_e32 v132, v16
	v_mfma_f32_32x32x16_bf16 v[18:33], v[118:121], v[158:161], v[18:33]
	v_exp_f32_e32 v2, v2
	v_exp_f32_e32 v6, v6
	v_exp_f32_e32 v10, v10
	v_exp_f32_e32 v12, v14
	v_fma_f32 v4, v131, s12, s12
	v_fma_f32 v8, v130, s12, s12
	v_fma_f32 v14, v133, s12, s12
	v_fma_f32 v16, v132, s12, s12
	v_mfma_f32_32x32x16_bf16 v[18:33], v[114:117], v[142:145], v[18:33]
	v_exp_f32_e32 v3, v3
	v_fmac_f32_e32 v4, v2, v4
	v_exp_f32_e32 v2, v7
	v_fmac_f32_e32 v8, v6, v8
	v_exp_f32_e32 v6, v11
	v_exp_f32_e32 v7, v15
	v_fmac_f32_e32 v14, v10, v14
	v_fmac_f32_e32 v16, v12, v16
	v_mfma_f32_32x32x16_bf16 v[18:33], v[110:113], v[154:157], v[18:33]
	v_add_f32_e32 v10, 1.0, v3
	v_rcp_f32_e32 v3, v4
	v_add_f32_e32 v4, 1.0, v2
	v_rcp_f32_e32 v2, v8
	v_rcp_f32_e32 v163, v14
	v_rcp_f32_e32 v162, v16
	v_mfma_f32_32x32x16_bf16 v[18:33], v[106:109], v[182:185], v[18:33]
	v_add_f32_e32 v6, 1.0, v6
	v_add_f32_e32 v7, 1.0, v7
	v_rcp_f32_e32 v167, v10
	v_rcp_f32_e32 v166, v4
	v_exp_f32_e32 v170, v5
	v_exp_f32_e32 v171, v9
	v_mfma_f32_32x32x16_bf16 v[18:33], v[102:105], v[186:189], v[18:33]
	v_rcp_f32_e32 v169, v6
	v_rcp_f32_e32 v168, v7
	v_exp_f32_e32 v172, v13
	v_exp_f32_e32 v173, v17
	v_mfma_f32_32x32x16_bf16 v[18:33], v[98:101], v[134:137], v[18:33]
	v_fma_f32 v130, -v130, v2, v2
	v_fma_f32 v131, -v131, v3, v3
	v_pk_fma_f32 v[204:205], v[166:167], v[224:225], v[130:131]
	s_nop 0
	v_pk_fma_f32 v[130:131], v[132:133], v[162:163], v[162:163] neg_lo:[1,0,0] neg_hi:[1,0,0]
	s_nop 0
	v_pk_fma_f32 v[202:203], v[168:169], v[226:227], v[130:131]
	s_waitcnt lgkmcnt(3)
	v_mfma_f32_32x32x16_bf16 v[18:33], v[94:97], v[138:141], v[18:33]
	v_add_f32_e32 v130, 1.0, v170
	v_exp_f32_e32 v131, v205
	v_add_f32_e32 v132, 1.0, v171
	v_exp_f32_e32 v133, v204
	v_exp_f32_e32 v162, v203
	v_exp_f32_e32 v163, v202
	v_add_f32_e32 v164, 1.0, v172
	v_add_f32_e32 v165, 1.0, v173
	s_waitcnt lgkmcnt(2)
	v_mfma_f32_32x32x16_bf16 v[18:33], v[90:93], v[146:149], v[18:33]
	v_fmac_f32_e32 v130, v130, v131
	v_fmac_f32_e32 v132, v132, v133
	v_fmac_f32_e32 v164, v164, v162
	v_fmac_f32_e32 v165, v165, v163
	s_waitcnt lgkmcnt(1)
	v_mfma_f32_32x32x16_bf16 v[18:33], v[86:89], v[150:153], v[18:33]
	v_rcp_f32_e32 v130, v130
	v_rcp_f32_e32 v132, v132
	v_rcp_f32_e32 v164, v164
	v_rcp_f32_e32 v165, v165
	s_waitcnt lgkmcnt(0)
	v_mfma_f32_32x32x16_bf16 v[18:33], v[82:85], v[178:181], v[18:33]
	v_fma_f32 v130, -v131, v130, v130
	v_fma_f32 v131, -v133, v132, v132
	v_fma_f32 v132, -v162, v164, v164
	v_fma_f32 v133, -v163, v165, v165
	v_cvt_pk_bf16_f32 v254, v130, v131
	v_cvt_pk_bf16_f32 v255, v132, v133
	ds_write_b128 v211, v[252:255] offset:0
	s_waitcnt lgkmcnt(0)
	s_barrier
	s_branch .LBB1_13

.Llight_path:
	s_waitcnt vmcnt(16)
	v_mul_u32_u24_e32 v236, 36, v228
	v_add_u32_e32 v236, v236, v230
	v_add_u32_e32 v237, s7, v229
	v_mul_u32_u24_e32 v238, 0x104, v228
	v_add_u32_e32 v238, v238, v237
	v_add_u32_e32 v238, 0xb840, v238
	ds_read_b128 v[2:5], v237 offset:36928
	ds_read_b128 v[6:9], v237 offset:36944
	ds_read_b128 v[10:13], v237 offset:36960
	ds_read_b128 v[14:17], v237 offset:36976
	ds_read_b128 v[18:21], v237 offset:37056
	ds_read_b128 v[22:25], v237 offset:37072
	ds_read_b128 v[26:29], v237 offset:37088
	ds_read_b128 v[30:33], v237 offset:37104
	ds_read_b128 v[162:165], v236 offset:16384
	ds_read_b128 v[166:169], v236 offset:16416
	ds_read_b128 v[170:173], v236 offset:16448
	ds_read_b128 v[174:177], v236 offset:16480
	s_waitcnt lgkmcnt(0)
	v_mfma_f32_32x32x16_bf16 v[2:17], v[94:97], v[162:165], v[2:17]
	v_mfma_f32_32x32x16_bf16 v[2:17], v[90:93], v[166:169], v[2:17]
	v_mfma_f32_32x32x16_bf16 v[2:17], v[86:89], v[170:173], v[2:17]
	v_mfma_f32_32x32x16_bf16 v[2:17], v[82:85], v[174:177], v[2:17]
	v_mfma_f32_32x32x16_bf16 v[18:33], v[46:49], v[162:165], v[18:33]
	ds_read_b128 v[130:133], v237 offset:36928
	ds_read_b128 v[134:137], v237 offset:36944
	ds_read_b128 v[138:141], v237 offset:36960
	v_mfma_f32_32x32x16_bf16 v[18:33], v[42:45], v[166:169], v[18:33]
	ds_read_b128 v[142:145], v237 offset:36976
	ds_read_b128 v[146:149], v237 offset:37056
	ds_read_b128 v[150:153], v237 offset:37072
	v_mfma_f32_32x32x16_bf16 v[18:33], v[38:41], v[170:173], v[18:33]
	ds_read_b128 v[154:157], v237 offset:37088
	ds_read_b128 v[158:161], v237 offset:37104
	ds_read_b128 v[178:181], v236 offset:20992
	v_mfma_f32_32x32x16_bf16 v[18:33], v[34:37], v[174:177], v[18:33]
	ds_read_b128 v[182:185], v236 offset:21024
	ds_read_b128 v[186:189], v236 offset:21056
	ds_read_b128 v[190:193], v236 offset:21088
	s_waitcnt lgkmcnt(0)
	v_mfma_f32_32x32x16_bf16 v[130:145], v[94:97], v[178:181], v[130:145]
	v_mfma_f32_32x32x16_bf16 v[130:145], v[90:93], v[182:185], v[130:145]
	v_mfma_f32_32x32x16_bf16 v[130:145], v[86:89], v[186:189], v[130:145]
	v_mfma_f32_32x32x16_bf16 v[130:145], v[82:85], v[190:193], v[130:145]
	s_nop 7
	ds_write_b128 v238, v[2:5] offset:0
	ds_write_b128 v238, v[6:9] offset:16
	ds_write_b128 v238, v[10:13] offset:32
	ds_write_b128 v238, v[14:17] offset:48
	ds_write_b128 v238, v[18:21] offset:128
	ds_write_b128 v238, v[22:25] offset:144
	ds_write_b128 v238, v[26:29] offset:160
	ds_write_b128 v238, v[30:33] offset:176
	v_mfma_f32_32x32x16_bf16 v[146:161], v[46:49], v[178:181], v[146:161]
	ds_read_b128 v[2:5], v237 offset:36928
	ds_read_b128 v[6:9], v237 offset:36944
	ds_read_b128 v[10:13], v237 offset:36960
	v_mfma_f32_32x32x16_bf16 v[146:161], v[42:45], v[182:185], v[146:161]
	ds_read_b128 v[14:17], v237 offset:36976
	ds_read_b128 v[18:21], v237 offset:37056
	ds_read_b128 v[22:25], v237 offset:37072
	v_mfma_f32_32x32x16_bf16 v[146:161], v[38:41], v[186:189], v[146:161]
	ds_read_b128 v[26:29], v237 offset:37088
	ds_read_b128 v[30:33], v237 offset:37104
	ds_read_b128 v[162:165], v236 offset:25600
	v_mfma_f32_32x32x16_bf16 v[146:161], v[34:37], v[190:193], v[146:161]
	ds_read_b128 v[166:169], v236 offset:25632
	ds_read_b128 v[170:173], v236 offset:25664
	ds_read_b128 v[174:177], v236 offset:25696
	s_waitcnt lgkmcnt(0)
	v_mfma_f32_32x32x16_bf16 v[2:17], v[94:97], v[162:165], v[2:17]
	v_mfma_f32_32x32x16_bf16 v[2:17], v[90:93], v[166:169], v[2:17]
	v_mfma_f32_32x32x16_bf16 v[2:17], v[86:89], v[170:173], v[2:17]
	v_mfma_f32_32x32x16_bf16 v[2:17], v[82:85], v[174:177], v[2:17]
	s_nop 7
	v_add_u32_e32 v239, 0x8200, v238
	ds_write_b128 v239, v[130:133] offset:0
	ds_write_b128 v239, v[134:137] offset:16
	ds_write_b128 v239, v[138:141] offset:32
	ds_write_b128 v239, v[142:145] offset:48
	ds_write_b128 v239, v[146:149] offset:128
	ds_write_b128 v239, v[150:153] offset:144
	ds_write_b128 v239, v[154:157] offset:160
	ds_write_b128 v239, v[158:161] offset:176
	v_mfma_f32_32x32x16_bf16 v[18:33], v[46:49], v[162:165], v[18:33]
	ds_read_b128 v[130:133], v237 offset:36928
	ds_read_b128 v[134:137], v237 offset:36944
	ds_read_b128 v[138:141], v237 offset:36960
	v_mfma_f32_32x32x16_bf16 v[18:33], v[42:45], v[166:169], v[18:33]
	ds_read_b128 v[142:145], v237 offset:36976
	ds_read_b128 v[146:149], v237 offset:37056
	ds_read_b128 v[150:153], v237 offset:37072
	v_mfma_f32_32x32x16_bf16 v[18:33], v[38:41], v[170:173], v[18:33]
	ds_read_b128 v[154:157], v237 offset:37088
	ds_read_b128 v[158:161], v237 offset:37104
	ds_read_b128 v[178:181], v236 offset:30208
	v_mfma_f32_32x32x16_bf16 v[18:33], v[34:37], v[174:177], v[18:33]
	ds_read_b128 v[182:185], v236 offset:30240
	ds_read_b128 v[186:189], v236 offset:30272
	ds_read_b128 v[190:193], v236 offset:30304
	s_waitcnt lgkmcnt(0)
	v_mfma_f32_32x32x16_bf16 v[130:145], v[94:97], v[178:181], v[130:145]
	v_mfma_f32_32x32x16_bf16 v[130:145], v[90:93], v[182:185], v[130:145]
	v_mfma_f32_32x32x16_bf16 v[130:145], v[86:89], v[186:189], v[130:145]
	v_mfma_f32_32x32x16_bf16 v[130:145], v[82:85], v[190:193], v[130:145]
	s_nop 7
	v_add_u32_e32 v239, 0x10400, v238
	ds_write_b128 v239, v[2:5] offset:0
	ds_write_b128 v239, v[6:9] offset:16
	ds_write_b128 v239, v[10:13] offset:32
	ds_write_b128 v239, v[14:17] offset:48
	ds_write_b128 v239, v[18:21] offset:128
	ds_write_b128 v239, v[22:25] offset:144
	ds_write_b128 v239, v[26:29] offset:160
	ds_write_b128 v239, v[30:33] offset:176
	v_mfma_f32_32x32x16_bf16 v[146:161], v[46:49], v[178:181], v[146:161]
	v_mfma_f32_32x32x16_bf16 v[146:161], v[42:45], v[182:185], v[146:161]
	v_mfma_f32_32x32x16_bf16 v[146:161], v[38:41], v[186:189], v[146:161]
	v_mfma_f32_32x32x16_bf16 v[146:161], v[34:37], v[190:193], v[146:161]
	s_nop 7
	s_nop 7
	v_cmp_gt_u32_e32 vcc, 16, v228
	s_and_saveexec_b64 s[20:21], vcc
	v_add_u32_e32 v239, 0x18600, v238
	ds_write_b128 v239, v[130:133] offset:0
	ds_write_b128 v239, v[134:137] offset:16
	ds_write_b128 v239, v[138:141] offset:32
	ds_write_b128 v239, v[142:145] offset:48
	ds_write_b128 v239, v[146:149] offset:128
	ds_write_b128 v239, v[150:153] offset:144
	ds_write_b128 v239, v[154:157] offset:160
	ds_write_b128 v239, v[158:161] offset:176
	s_or_b64 exec, exec, s[20:21]
	s_waitcnt vmcnt(0) lgkmcnt(0)
	s_nop 7
	s_nop 7
	s_waitcnt vmcnt(0)
	v_add_u32_e32 v231, s7, v229
	v_add_u32_e32 v231, 0xb840, v231
	v_add_u32_e32 v211, s6, v210
	s_mov_b32 s12, 0xbeb17218
	v_mov_b32_e32 v235, 0xc038aa3b
	s_nop 0
	s_load_dwordx8 s[4:11], s[0:1], 0x10
	s_waitcnt lgkmcnt(0)
	v_add_u32_e32 v232, 0x24e80, v228
	ds_read_b32 v244, v232
	ds_read_b32 v245, v232 offset:128
	v_mov_b32_e32 v194, 0
	v_mov_b32_e32 v195, 0
	v_mov_b32_e32 v196, 0
	v_mov_b32_e32 v197, 0
	v_mov_b32_e32 v198, 0
	v_mov_b32_e32 v199, 0
	v_mov_b32_e32 v200, 0
	v_mov_b32_e32 v201, 0
	v_mov_b32_e32 v202, 0
	v_mov_b32_e32 v203, 0
	v_mov_b32_e32 v204, 0
	v_mov_b32_e32 v205, 0
	v_mov_b32_e32 v206, 0
	v_mov_b32_e32 v207, 0
	v_mov_b32_e32 v208, 0
	v_mov_b32_e32 v209, 0
	v_add_u32_e32 v232, 0x100, v232
	s_waitcnt lgkmcnt(0)
	v_add_u32_e32 v233, v231, v244
	v_add_u32_e32 v234, v231, v245
	ds_read_b128 v[2:5], v233 offset:0
	ds_read_b128 v[6:9], v233 offset:16
	ds_read_b128 v[10:13], v233 offset:32
	ds_read_b128 v[14:17], v233 offset:48
	ds_read_b128 v[18:21], v233 offset:128
	ds_read_b128 v[22:25], v233 offset:144
	ds_read_b128 v[26:29], v233 offset:160
	ds_read_b128 v[30:33], v233 offset:176
	ds_read_b128 v[34:37], v234 offset:0
	ds_read_b128 v[38:41], v234 offset:16
	ds_read_b128 v[42:45], v234 offset:32
	ds_read_b128 v[46:49], v234 offset:48
	s_movk_i32 s16, 18
	s_waitcnt lgkmcnt(0)
	ds_read_b128 v[82:85], v234 offset:128
	ds_read_b128 v[86:89], v234 offset:144
	ds_read_b128 v[90:93], v234 offset:160
	ds_read_b128 v[94:97], v234 offset:176
	ds_read2_b32 v[244:245], v232 offset1:32
	v_exp_f32_e32 v212, v4
	v_exp_f32_e32 v213, v8
	v_exp_f32_e32 v214, v12
	v_exp_f32_e32 v215, v16
	v_exp_f32_e32 v217, v2
	v_fma_f32 v251, v212, s12, s12
	v_exp_f32_e32 v218, v6
	v_fma_f32 v252, v213, s12, s12
	v_exp_f32_e32 v219, v10
	v_fma_f32 v253, v214, s12, s12
	v_exp_f32_e32 v220, v14
	v_fma_f32 v254, v215, s12, s12
	v_fmac_f32_e32 v251, v217, v251
	v_fmac_f32_e32 v252, v218, v252
	v_fmac_f32_e32 v253, v219, v253
	v_fmac_f32_e32 v254, v220, v254
	v_rcp_f32_e32 v217, v251
	v_rcp_f32_e32 v218, v252
	v_rcp_f32_e32 v219, v253
	v_rcp_f32_e32 v220, v254
	v_exp_f32_e32 v246, v5
	v_fma_f32 v194, -v212, v217, v217
	v_exp_f32_e32 v247, v9
	v_fma_f32 v195, -v213, v218, v218
	v_exp_f32_e32 v248, v13
	v_fma_f32 v196, -v214, v219, v219
	v_exp_f32_e32 v249, v17
	v_fma_f32 v197, -v215, v220, v220
	v_exp_f32_e32 v212, v194
	v_add_f32_e32 v246, 1.0, v246
	v_exp_f32_e32 v213, v195
	v_add_f32_e32 v247, 1.0, v247
	v_exp_f32_e32 v214, v196
	v_add_f32_e32 v248, 1.0, v248
	v_exp_f32_e32 v215, v197
	v_add_f32_e32 v249, 1.0, v249
	v_fmac_f32_e32 v246, v246, v212
	v_fmac_f32_e32 v247, v247, v213
	v_fmac_f32_e32 v248, v248, v214
	v_fmac_f32_e32 v249, v249, v215
	v_rcp_f32_e32 v246, v246
	v_rcp_f32_e32 v247, v247
	v_rcp_f32_e32 v248, v248
	v_rcp_f32_e32 v249, v249
	v_fma_f32 v246, -v212, v246, v246
	v_fma_f32 v247, -v213, v247, v247
	v_fma_f32 v248, -v214, v248, v248
	v_fma_f32 v249, -v215, v249, v249
	v_cvt_pk_bf16_f32 v236, v246, v247
	v_cvt_pk_bf16_f32 v237, v248, v249
	s_waitcnt lgkmcnt(0)
	v_add_u32_e32 v233, v231, v244
	ds_read_b128 v[2:5], v233 offset:0
	ds_read_b128 v[6:9], v233 offset:16
	ds_read_b128 v[10:13], v233 offset:32
	ds_read_b128 v[14:17], v233 offset:48
	v_exp_f32_e32 v212, v20
	v_exp_f32_e32 v213, v24
	v_exp_f32_e32 v214, v28
	v_exp_f32_e32 v215, v32
	v_exp_f32_e32 v217, v18
	v_fma_f32 v251, v212, s12, s12
	v_exp_f32_e32 v218, v22
	v_fma_f32 v252, v213, s12, s12
	v_exp_f32_e32 v219, v26
	v_fma_f32 v253, v214, s12, s12
	v_exp_f32_e32 v220, v30
	v_fma_f32 v254, v215, s12, s12
	v_fmac_f32_e32 v251, v217, v251
	v_fmac_f32_e32 v252, v218, v252
	v_fmac_f32_e32 v253, v219, v253
	v_fmac_f32_e32 v254, v220, v254
	v_rcp_f32_e32 v217, v251
	v_rcp_f32_e32 v218, v252
	v_rcp_f32_e32 v219, v253
	v_rcp_f32_e32 v220, v254
	v_exp_f32_e32 v246, v21
	v_fma_f32 v198, -v212, v217, v217
	v_exp_f32_e32 v247, v25
	v_fma_f32 v199, -v213, v218, v218
	v_exp_f32_e32 v248, v29
	v_fma_f32 v200, -v214, v219, v219
	v_exp_f32_e32 v249, v33
	v_fma_f32 v201, -v215, v220, v220
	v_exp_f32_e32 v212, v198
	v_add_f32_e32 v246, 1.0, v246
	v_exp_f32_e32 v213, v199
	v_add_f32_e32 v247, 1.0, v247
	v_exp_f32_e32 v214, v200
	v_add_f32_e32 v248, 1.0, v248
	v_exp_f32_e32 v215, v201
	v_add_f32_e32 v249, 1.0, v249
	v_fmac_f32_e32 v246, v246, v212
	v_fmac_f32_e32 v247, v247, v213
	v_fmac_f32_e32 v248, v248, v214
	v_fmac_f32_e32 v249, v249, v215
	v_rcp_f32_e32 v246, v246
	v_rcp_f32_e32 v247, v247
	v_rcp_f32_e32 v248, v248
	v_rcp_f32_e32 v249, v249
	v_fma_f32 v246, -v212, v246, v246
	v_fma_f32 v247, -v213, v247, v247
	v_fma_f32 v248, -v214, v248, v248
	v_fma_f32 v249, -v215, v249, v249
	v_cvt_pk_bf16_f32 v238, v246, v247
	v_cvt_pk_bf16_f32 v239, v248, v249
	ds_write_b128 v211, v[236:239] offset:0
	s_waitcnt lgkmcnt(0)
	s_barrier
	ds_read_b128 v[130:133], v210 offset:0
	ds_read_b128 v[134:137], v210 offset:1024
	ds_read_b128 v[18:21], v233 offset:128
	ds_read_b128 v[22:25], v233 offset:144
	ds_read_b128 v[26:29], v233 offset:160
	ds_read_b128 v[30:33], v233 offset:176
	v_exp_f32_e32 v212, v36
	v_exp_f32_e32 v213, v40
	v_exp_f32_e32 v214, v44
	v_exp_f32_e32 v215, v48
	ds_read_b128 v[138:141], v210 offset:2048
	ds_read_b128 v[142:145], v210 offset:3072
	v_exp_f32_e32 v217, v34
	v_fma_f32 v251, v212, s12, s12
	v_exp_f32_e32 v218, v38
	v_fma_f32 v252, v213, s12, s12
	v_exp_f32_e32 v219, v42
	v_fma_f32 v253, v214, s12, s12
	v_exp_f32_e32 v220, v46
	v_fma_f32 v254, v215, s12, s12
	ds_read_b128 v[146:149], v210 offset:4096
	ds_read_b128 v[150:153], v210 offset:5120
	v_fmac_f32_e32 v251, v217, v251
	v_fmac_f32_e32 v252, v218, v252
	v_fmac_f32_e32 v253, v219, v253
	v_fmac_f32_e32 v254, v220, v254
	ds_read_b128 v[154:157], v210 offset:6144
	ds_read_b128 v[158:161], v210 offset:7168
	v_rcp_f32_e32 v217, v251
	v_rcp_f32_e32 v218, v252
	v_rcp_f32_e32 v219, v253
	v_rcp_f32_e32 v220, v254
	v_exp_f32_e32 v246, v37
	v_fma_f32 v202, -v212, v217, v217
	v_exp_f32_e32 v247, v41
	v_fma_f32 v203, -v213, v218, v218
	v_exp_f32_e32 v248, v45
	v_fma_f32 v204, -v214, v219, v219
	v_exp_f32_e32 v249, v49
	v_fma_f32 v205, -v215, v220, v220
	v_exp_f32_e32 v212, v202
	v_add_f32_e32 v246, 1.0, v246
	v_exp_f32_e32 v213, v203
	v_add_f32_e32 v247, 1.0, v247
	v_exp_f32_e32 v214, v204
	v_add_f32_e32 v248, 1.0, v248
	v_exp_f32_e32 v215, v205
	v_add_f32_e32 v249, 1.0, v249
	v_fmac_f32_e32 v246, v246, v212
	v_fmac_f32_e32 v247, v247, v213
	v_fmac_f32_e32 v248, v248, v214
	v_fmac_f32_e32 v249, v249, v215
	v_rcp_f32_e32 v246, v246
	v_rcp_f32_e32 v247, v247
	v_rcp_f32_e32 v248, v248
	v_rcp_f32_e32 v249, v249
	v_fma_f32 v246, -v212, v246, v246
	v_fma_f32 v247, -v213, v247, v247
	v_fma_f32 v248, -v214, v248, v248
	v_fma_f32 v249, -v215, v249, v249
	v_cvt_pk_bf16_f32 v236, v246, v247
	v_cvt_pk_bf16_f32 v237, v248, v249
	s_waitcnt lgkmcnt(0)
	v_mfma_f32_32x32x16_bf16 v[2:17], v[126:129], v[130:133], v[2:17]
	v_add_u32_e32 v234, v231, v245
	ds_read_b128 v[34:37], v234 offset:0
	ds_read_b128 v[38:41], v234 offset:16
	ds_read_b128 v[42:45], v234 offset:32
	ds_read_b128 v[46:49], v234 offset:48
	v_add_u32_e32 v232, 0x100, v232
	v_exp_f32_e32 v212, v84
	v_exp_f32_e32 v213, v88
	v_exp_f32_e32 v214, v92
	v_exp_f32_e32 v215, v96
	v_mfma_f32_32x32x16_bf16 v[2:17], v[122:125], v[134:137], v[2:17]
	v_exp_f32_e32 v217, v82
	v_fma_f32 v251, v212, s12, s12
	v_exp_f32_e32 v218, v86
	v_fma_f32 v252, v213, s12, s12
	v_exp_f32_e32 v219, v90
	v_fma_f32 v253, v214, s12, s12
	v_exp_f32_e32 v220, v94
	v_fma_f32 v254, v215, s12, s12
	v_mfma_f32_32x32x16_bf16 v[2:17], v[118:121], v[138:141], v[2:17]
	v_fmac_f32_e32 v251, v217, v251
	v_fmac_f32_e32 v252, v218, v252
	v_fmac_f32_e32 v253, v219, v253
	v_fmac_f32_e32 v254, v220, v254
	v_mfma_f32_32x32x16_bf16 v[2:17], v[114:117], v[142:145], v[2:17]
	v_rcp_f32_e32 v217, v251
	v_rcp_f32_e32 v218, v252
	v_rcp_f32_e32 v219, v253
	v_rcp_f32_e32 v220, v254
	v_mfma_f32_32x32x16_bf16 v[2:17], v[110:113], v[146:149], v[2:17]
	v_exp_f32_e32 v246, v85
	v_fma_f32 v206, -v212, v217, v217
	v_exp_f32_e32 v247, v89
	v_fma_f32 v207, -v213, v218, v218
	v_exp_f32_e32 v248, v93
	v_fma_f32 v208, -v214, v219, v219
	v_exp_f32_e32 v249, v97
	v_fma_f32 v209, -v215, v220, v220
	v_mfma_f32_32x32x16_bf16 v[2:17], v[106:109], v[150:153], v[2:17]
	v_mfma_f32_32x32x16_bf16 v[2:17], v[102:105], v[154:157], v[2:17]
	v_exp_f32_e32 v212, v206
	v_add_f32_e32 v246, 1.0, v246
	v_exp_f32_e32 v213, v207
	v_add_f32_e32 v247, 1.0, v247
	v_exp_f32_e32 v214, v208
	v_add_f32_e32 v248, 1.0, v248
	v_exp_f32_e32 v215, v209
	v_add_f32_e32 v249, 1.0, v249
	v_fmac_f32_e32 v246, v246, v212
	v_fmac_f32_e32 v247, v247, v213
	v_fmac_f32_e32 v248, v248, v214
	v_fmac_f32_e32 v249, v249, v215
	v_mfma_f32_32x32x16_bf16 v[2:17], v[98:101], v[158:161], v[2:17]
	v_rcp_f32_e32 v246, v246
	v_rcp_f32_e32 v247, v247
	v_rcp_f32_e32 v248, v248
	v_rcp_f32_e32 v249, v249
	v_fma_f32 v246, -v212, v246, v246
	v_fma_f32 v247, -v213, v247, v247
	v_fma_f32 v248, -v214, v248, v248
	v_fma_f32 v249, -v215, v249, v249
	v_cvt_pk_bf16_f32 v238, v246, v247
	v_cvt_pk_bf16_f32 v239, v248, v249
	ds_write_b128 v211, v[236:239] offset:8192
	s_waitcnt lgkmcnt(0)
	s_barrier
	.p2align 6
.Llight_loop:
	v_mfma_f32_32x32x16_bf16 v[18:33], v[78:81], v[130:133], v[18:33]
	ds_read_b128 v[162:165], v210 offset:8192
	ds_read_b128 v[166:169], v210 offset:9216
	ds_read_b128 v[82:85], v234 offset:128
	ds_read_b128 v[86:89], v234 offset:144
	ds_read_b128 v[90:93], v234 offset:160
	ds_read_b128 v[94:97], v234 offset:176
	ds_read2_b32 v[244:245], v232 offset1:32
	v_exp_f32_e32 v212, v4
	v_exp_f32_e32 v213, v8
	v_exp_f32_e32 v214, v12
	v_exp_f32_e32 v215, v16
	v_mfma_f32_32x32x16_bf16 v[18:33], v[74:77], v[134:137], v[18:33]
	ds_read_b128 v[170:173], v210 offset:10240
	ds_read_b128 v[174:177], v210 offset:11264
	v_exp_f32_e32 v217, v2
	v_fma_f32 v251, v212, s12, s12
	v_exp_f32_e32 v218, v6
	v_fma_f32 v252, v213, s12, s12
	v_exp_f32_e32 v219, v10
	v_fma_f32 v253, v214, s12, s12
	v_exp_f32_e32 v220, v14
	v_fma_f32 v254, v215, s12, s12
	v_mfma_f32_32x32x16_bf16 v[18:33], v[70:73], v[138:141], v[18:33]
	ds_read_b128 v[178:181], v210 offset:12288
	ds_read_b128 v[182:185], v210 offset:13312
	v_exp_f32_e32 v221, v3
	v_fmac_f32_e32 v251, v217, v251
	v_exp_f32_e32 v222, v7
	v_fmac_f32_e32 v252, v218, v252
	v_exp_f32_e32 v223, v11
	v_fmac_f32_e32 v253, v219, v253
	v_exp_f32_e32 v224, v15
	v_fmac_f32_e32 v254, v220, v254
	v_mfma_f32_32x32x16_bf16 v[18:33], v[66:69], v[142:145], v[18:33]
	ds_read_b128 v[186:189], v210 offset:14336
	ds_read_b128 v[190:193], v210 offset:15360
	v_rcp_f32_e32 v217, v251
	v_add_f32_e32 v221, 1.0, v221
	v_rcp_f32_e32 v218, v252
	v_add_f32_e32 v222, 1.0, v222
	v_rcp_f32_e32 v219, v253
	v_add_f32_e32 v223, 1.0, v223
	v_rcp_f32_e32 v220, v254
	v_add_f32_e32 v224, 1.0, v224
	v_mfma_f32_32x32x16_bf16 v[18:33], v[62:65], v[146:149], v[18:33]
	v_rcp_f32_e32 v221, v221
	v_fma_f32 v240, -v212, v217, v217
	v_rcp_f32_e32 v222, v222
	v_fma_f32 v241, -v213, v218, v218
	v_rcp_f32_e32 v223, v223
	v_fma_f32 v242, -v214, v219, v219
	v_rcp_f32_e32 v224, v224
	v_fma_f32 v243, -v215, v220, v220
	v_mfma_f32_32x32x16_bf16 v[18:33], v[58:61], v[150:153], v[18:33]
	v_exp_f32_e32 v246, v5
	v_fma_f32 v194, v221, v194, v240
	v_exp_f32_e32 v247, v9
	v_fma_f32 v195, v222, v195, v241
	v_exp_f32_e32 v248, v13
	v_fma_f32 v196, v223, v196, v242
	v_exp_f32_e32 v249, v17
	v_fma_f32 v197, v224, v197, v243
	v_mfma_f32_32x32x16_bf16 v[18:33], v[54:57], v[154:157], v[18:33]
	v_exp_f32_e32 v212, v194
	v_add_f32_e32 v246, 1.0, v246
	v_exp_f32_e32 v213, v195
	v_add_f32_e32 v247, 1.0, v247
	v_exp_f32_e32 v214, v196
	v_add_f32_e32 v248, 1.0, v248
	v_exp_f32_e32 v215, v197
	v_add_f32_e32 v249, 1.0, v249
	v_fmac_f32_e32 v246, v246, v212
	v_fmac_f32_e32 v247, v247, v213
	v_fmac_f32_e32 v248, v248, v214
	v_fmac_f32_e32 v249, v249, v215
	v_mfma_f32_32x32x16_bf16 v[18:33], v[50:53], v[158:161], v[18:33]
	v_rcp_f32_e32 v246, v246
	v_rcp_f32_e32 v247, v247
	v_rcp_f32_e32 v248, v248
	v_rcp_f32_e32 v249, v249
	v_fma_f32 v246, -v212, v246, v246
	v_fma_f32 v247, -v213, v247, v247
	v_fma_f32 v248, -v214, v248, v248
	v_fma_f32 v249, -v215, v249, v249
	v_cvt_pk_bf16_f32 v236, v246, v247
	v_cvt_pk_bf16_f32 v237, v248, v249
	s_waitcnt lgkmcnt(0)
	v_mfma_f32_32x32x16_bf16 v[34:49], v[126:129], v[162:165], v[34:49]
	v_add_u32_e32 v233, v231, v244
	ds_read_b128 v[2:5], v233 offset:0
	ds_read_b128 v[6:9], v233 offset:16
	ds_read_b128 v[10:13], v233 offset:32
	ds_read_b128 v[14:17], v233 offset:48
	v_exp_f32_e32 v212, v20
	v_exp_f32_e32 v213, v24
	v_exp_f32_e32 v214, v28
	v_exp_f32_e32 v215, v32
	v_mfma_f32_32x32x16_bf16 v[34:49], v[122:125], v[166:169], v[34:49]
	v_exp_f32_e32 v217, v18
	v_fma_f32 v251, v212, s12, s12
	v_exp_f32_e32 v218, v22
	v_fma_f32 v252, v213, s12, s12
	v_exp_f32_e32 v219, v26
	v_fma_f32 v253, v214, s12, s12
	v_exp_f32_e32 v220, v30
	v_fma_f32 v254, v215, s12, s12
	v_mfma_f32_32x32x16_bf16 v[34:49], v[118:121], v[170:173], v[34:49]
	v_exp_f32_e32 v221, v19
	v_fmac_f32_e32 v251, v217, v251
	v_exp_f32_e32 v222, v23
	v_fmac_f32_e32 v252, v218, v252
	v_exp_f32_e32 v223, v27
	v_fmac_f32_e32 v253, v219, v253
	v_exp_f32_e32 v224, v31
	v_fmac_f32_e32 v254, v220, v254
	v_mfma_f32_32x32x16_bf16 v[34:49], v[114:117], v[174:177], v[34:49]
	v_rcp_f32_e32 v217, v251
	v_add_f32_e32 v221, 1.0, v221
	v_rcp_f32_e32 v218, v252
	v_add_f32_e32 v222, 1.0, v222
	v_rcp_f32_e32 v219, v253
	v_add_f32_e32 v223, 1.0, v223
	v_rcp_f32_e32 v220, v254
	v_add_f32_e32 v224, 1.0, v224
	v_mfma_f32_32x32x16_bf16 v[34:49], v[110:113], v[178:181], v[34:49]
	v_rcp_f32_e32 v221, v221
	v_fma_f32 v240, -v212, v217, v217
	v_rcp_f32_e32 v222, v222
	v_fma_f32 v241, -v213, v218, v218
	v_rcp_f32_e32 v223, v223
	v_fma_f32 v242, -v214, v219, v219
	v_rcp_f32_e32 v224, v224
	v_fma_f32 v243, -v215, v220, v220
	v_mfma_f32_32x32x16_bf16 v[34:49], v[106:109], v[182:185], v[34:49]
	v_exp_f32_e32 v246, v21
	v_fma_f32 v198, v221, v198, v240
	v_exp_f32_e32 v247, v25
	v_fma_f32 v199, v222, v199, v241
	v_exp_f32_e32 v248, v29
	v_fma_f32 v200, v223, v200, v242
	v_exp_f32_e32 v249, v33
	v_fma_f32 v201, v224, v201, v243
	v_mfma_f32_32x32x16_bf16 v[34:49], v[102:105], v[186:189], v[34:49]
	v_exp_f32_e32 v212, v198
	v_add_f32_e32 v246, 1.0, v246
	v_exp_f32_e32 v213, v199
	v_add_f32_e32 v247, 1.0, v247
	v_exp_f32_e32 v214, v200
	v_add_f32_e32 v248, 1.0, v248
	v_exp_f32_e32 v215, v201
	v_add_f32_e32 v249, 1.0, v249
	v_fmac_f32_e32 v246, v246, v212
	v_fmac_f32_e32 v247, v247, v213
	v_fmac_f32_e32 v248, v248, v214
	v_fmac_f32_e32 v249, v249, v215
	v_mfma_f32_32x32x16_bf16 v[34:49], v[98:101], v[190:193], v[34:49]
	v_rcp_f32_e32 v246, v246
	v_rcp_f32_e32 v247, v247
	v_rcp_f32_e32 v248, v248
	v_rcp_f32_e32 v249, v249
	v_fma_f32 v246, -v212, v246, v246
	v_fma_f32 v247, -v213, v247, v247
	v_fma_f32 v248, -v214, v248, v248
	v_fma_f32 v249, -v215, v249, v249
	v_cvt_pk_bf16_f32 v238, v246, v247
	v_cvt_pk_bf16_f32 v239, v248, v249
	ds_write_b128 v211, v[236:239] offset:0
	s_waitcnt lgkmcnt(0)
	s_barrier
	v_mfma_f32_32x32x16_bf16 v[82:97], v[78:81], v[162:165], v[82:97]
	ds_read_b128 v[130:133], v210 offset:0
	ds_read_b128 v[134:137], v210 offset:1024
	ds_read_b128 v[18:21], v233 offset:128
	ds_read_b128 v[22:25], v233 offset:144
	ds_read_b128 v[26:29], v233 offset:160
	ds_read_b128 v[30:33], v233 offset:176
	v_exp_f32_e32 v212, v36
	v_exp_f32_e32 v213, v40
	v_exp_f32_e32 v214, v44
	v_exp_f32_e32 v215, v48
	v_mfma_f32_32x32x16_bf16 v[82:97], v[74:77], v[166:169], v[82:97]
	ds_read_b128 v[138:141], v210 offset:2048
	ds_read_b128 v[142:145], v210 offset:3072
	v_exp_f32_e32 v217, v34
	v_fma_f32 v251, v212, s12, s12
	v_exp_f32_e32 v218, v38
	v_fma_f32 v252, v213, s12, s12
	v_exp_f32_e32 v219, v42
	v_fma_f32 v253, v214, s12, s12
	v_exp_f32_e32 v220, v46
	v_fma_f32 v254, v215, s12, s12
	v_mfma_f32_32x32x16_bf16 v[82:97], v[70:73], v[170:173], v[82:97]
	ds_read_b128 v[146:149], v210 offset:4096
	ds_read_b128 v[150:153], v210 offset:5120
	v_exp_f32_e32 v221, v35
	v_fmac_f32_e32 v251, v217, v251
	v_exp_f32_e32 v222, v39
	v_fmac_f32_e32 v252, v218, v252
	v_exp_f32_e32 v223, v43
	v_fmac_f32_e32 v253, v219, v253
	v_exp_f32_e32 v224, v47
	v_fmac_f32_e32 v254, v220, v254
	v_mfma_f32_32x32x16_bf16 v[82:97], v[66:69], v[174:177], v[82:97]
	ds_read_b128 v[154:157], v210 offset:6144
	ds_read_b128 v[158:161], v210 offset:7168
	v_rcp_f32_e32 v217, v251
	v_add_f32_e32 v221, 1.0, v221
	v_rcp_f32_e32 v218, v252
	v_add_f32_e32 v222, 1.0, v222
	v_rcp_f32_e32 v219, v253
	v_add_f32_e32 v223, 1.0, v223
	v_rcp_f32_e32 v220, v254
	v_add_f32_e32 v224, 1.0, v224
	v_mfma_f32_32x32x16_bf16 v[82:97], v[62:65], v[178:181], v[82:97]
	v_rcp_f32_e32 v221, v221
	v_fma_f32 v240, -v212, v217, v217
	v_rcp_f32_e32 v222, v222
	v_fma_f32 v241, -v213, v218, v218
	v_rcp_f32_e32 v223, v223
	v_fma_f32 v242, -v214, v219, v219
	v_rcp_f32_e32 v224, v224
	v_fma_f32 v243, -v215, v220, v220
	v_mfma_f32_32x32x16_bf16 v[82:97], v[58:61], v[182:185], v[82:97]
	v_exp_f32_e32 v246, v37
	v_fma_f32 v202, v221, v202, v240
	v_exp_f32_e32 v247, v41
	v_fma_f32 v203, v222, v203, v241
	v_exp_f32_e32 v248, v45
	v_fma_f32 v204, v223, v204, v242
	v_exp_f32_e32 v249, v49
	v_fma_f32 v205, v224, v205, v243
	v_mfma_f32_32x32x16_bf16 v[82:97], v[54:57], v[186:189], v[82:97]
	v_exp_f32_e32 v212, v202
	v_add_f32_e32 v246, 1.0, v246
	v_exp_f32_e32 v213, v203
	v_add_f32_e32 v247, 1.0, v247
	v_exp_f32_e32 v214, v204
	v_add_f32_e32 v248, 1.0, v248
	v_exp_f32_e32 v215, v205
	v_add_f32_e32 v249, 1.0, v249
	v_fmac_f32_e32 v246, v246, v212
	v_fmac_f32_e32 v247, v247, v213
	v_fmac_f32_e32 v248, v248, v214
	v_fmac_f32_e32 v249, v249, v215
	v_mfma_f32_32x32x16_bf16 v[82:97], v[50:53], v[190:193], v[82:97]
	v_rcp_f32_e32 v246, v246
	v_rcp_f32_e32 v247, v247
	v_rcp_f32_e32 v248, v248
	v_rcp_f32_e32 v249, v249
	v_fma_f32 v246, -v212, v246, v246
	v_fma_f32 v247, -v213, v247, v247
	v_fma_f32 v248, -v214, v248, v248
	v_fma_f32 v249, -v215, v249, v249
	v_cvt_pk_bf16_f32 v236, v246, v247
	v_cvt_pk_bf16_f32 v237, v248, v249
	s_waitcnt lgkmcnt(0)
	v_mfma_f32_32x32x16_bf16 v[2:17], v[126:129], v[130:133], v[2:17]
	v_add_u32_e32 v234, v231, v245
	ds_read_b128 v[34:37], v234 offset:0
	ds_read_b128 v[38:41], v234 offset:16
	ds_read_b128 v[42:45], v234 offset:32
	ds_read_b128 v[46:49], v234 offset:48
	v_add_u32_e32 v232, 0x100, v232
	v_exp_f32_e32 v212, v84
	v_exp_f32_e32 v213, v88
	v_exp_f32_e32 v214, v92
	v_exp_f32_e32 v215, v96
	v_mfma_f32_32x32x16_bf16 v[2:17], v[122:125], v[134:137], v[2:17]
	v_exp_f32_e32 v217, v82
	v_fma_f32 v251, v212, s12, s12
	v_exp_f32_e32 v218, v86
	v_fma_f32 v252, v213, s12, s12
	v_exp_f32_e32 v219, v90
	v_fma_f32 v253, v214, s12, s12
	v_exp_f32_e32 v220, v94
	v_fma_f32 v254, v215, s12, s12
	v_mfma_f32_32x32x16_bf16 v[2:17], v[118:121], v[138:141], v[2:17]
	v_exp_f32_e32 v221, v83
	v_fmac_f32_e32 v251, v217, v251
	v_exp_f32_e32 v222, v87
	v_fmac_f32_e32 v252, v218, v252
	v_exp_f32_e32 v223, v91
	v_fmac_f32_e32 v253, v219, v253
	v_exp_f32_e32 v224, v95
	v_fmac_f32_e32 v254, v220, v254
	v_mfma_f32_32x32x16_bf16 v[2:17], v[114:117], v[142:145], v[2:17]
	v_rcp_f32_e32 v217, v251
	v_add_f32_e32 v221, 1.0, v221
	v_rcp_f32_e32 v218, v252
	v_add_f32_e32 v222, 1.0, v222
	v_rcp_f32_e32 v219, v253
	v_add_f32_e32 v223, 1.0, v223
	v_rcp_f32_e32 v220, v254
	v_add_f32_e32 v224, 1.0, v224
	v_mfma_f32_32x32x16_bf16 v[2:17], v[110:113], v[146:149], v[2:17]
	v_rcp_f32_e32 v221, v221
	v_fma_f32 v240, -v212, v217, v217
	v_rcp_f32_e32 v222, v222
	v_fma_f32 v241, -v213, v218, v218
	v_rcp_f32_e32 v223, v223
	v_fma_f32 v242, -v214, v219, v219
	v_rcp_f32_e32 v224, v224
	v_fma_f32 v243, -v215, v220, v220
	v_mfma_f32_32x32x16_bf16 v[2:17], v[106:109], v[150:153], v[2:17]
	v_exp_f32_e32 v246, v85
	v_fma_f32 v206, v221, v206, v240
	v_exp_f32_e32 v247, v89
	v_fma_f32 v207, v222, v207, v241
	v_exp_f32_e32 v248, v93
	v_fma_f32 v208, v223, v208, v242
	v_exp_f32_e32 v249, v97
	v_fma_f32 v209, v224, v209, v243
	v_mfma_f32_32x32x16_bf16 v[2:17], v[102:105], v[154:157], v[2:17]
	v_exp_f32_e32 v212, v206
	v_add_f32_e32 v246, 1.0, v246
	v_exp_f32_e32 v213, v207
	v_add_f32_e32 v247, 1.0, v247
	v_exp_f32_e32 v214, v208
	v_add_f32_e32 v248, 1.0, v248
	v_exp_f32_e32 v215, v209
	v_add_f32_e32 v249, 1.0, v249
	v_fmac_f32_e32 v246, v246, v212
	v_fmac_f32_e32 v247, v247, v213
	v_fmac_f32_e32 v248, v248, v214
	v_fmac_f32_e32 v249, v249, v215
	v_mfma_f32_32x32x16_bf16 v[2:17], v[98:101], v[158:161], v[2:17]
	v_rcp_f32_e32 v246, v246
	v_rcp_f32_e32 v247, v247
	v_rcp_f32_e32 v248, v248
	v_rcp_f32_e32 v249, v249
	v_fma_f32 v246, -v212, v246, v246
	v_fma_f32 v247, -v213, v247, v247
	v_fma_f32 v248, -v214, v248, v248
	v_fma_f32 v249, -v215, v249, v249
	v_cvt_pk_bf16_f32 v238, v246, v247
	v_cvt_pk_bf16_f32 v239, v248, v249
	ds_write_b128 v211, v[236:239] offset:8192
	s_waitcnt lgkmcnt(0)
	s_barrier
	s_sub_u32 s16, s16, 1
	s_cmp_lg_u32 s16, 0
	s_cbranch_scc1 .Llight_loop
	v_mfma_f32_32x32x16_bf16 v[18:33], v[78:81], v[130:133], v[18:33]
	ds_read_b128 v[162:165], v210 offset:8192
	ds_read_b128 v[166:169], v210 offset:9216
	ds_read_b128 v[82:85], v234 offset:128
	ds_read_b128 v[86:89], v234 offset:144
	ds_read_b128 v[90:93], v234 offset:160
	ds_read_b128 v[94:97], v234 offset:176
	v_exp_f32_e32 v212, v4
	v_exp_f32_e32 v213, v8
	v_exp_f32_e32 v214, v12
	v_exp_f32_e32 v215, v16
	v_mfma_f32_32x32x16_bf16 v[18:33], v[74:77], v[134:137], v[18:33]
	ds_read_b128 v[170:173], v210 offset:10240
	ds_read_b128 v[174:177], v210 offset:11264
	v_exp_f32_e32 v217, v2
	v_fma_f32 v251, v212, s12, s12
	v_exp_f32_e32 v218, v6
	v_fma_f32 v252, v213, s12, s12
	v_exp_f32_e32 v219, v10
	v_fma_f32 v253, v214, s12, s12
	v_exp_f32_e32 v220, v14
	v_fma_f32 v254, v215, s12, s12
	v_mfma_f32_32x32x16_bf16 v[18:33], v[70:73], v[138:141], v[18:33]
	ds_read_b128 v[178:181], v210 offset:12288
	ds_read_b128 v[182:185], v210 offset:13312
	v_exp_f32_e32 v221, v3
	v_fmac_f32_e32 v251, v217, v251
	v_exp_f32_e32 v222, v7
	v_fmac_f32_e32 v252, v218, v252
	v_exp_f32_e32 v223, v11
	v_fmac_f32_e32 v253, v219, v253
	v_exp_f32_e32 v224, v15
	v_fmac_f32_e32 v254, v220, v254
	v_mfma_f32_32x32x16_bf16 v[18:33], v[66:69], v[142:145], v[18:33]
	ds_read_b128 v[186:189], v210 offset:14336
	ds_read_b128 v[190:193], v210 offset:15360
	v_rcp_f32_e32 v217, v251
	v_add_f32_e32 v221, 1.0, v221
	v_rcp_f32_e32 v218, v252
	v_add_f32_e32 v222, 1.0, v222
	v_rcp_f32_e32 v219, v253
	v_add_f32_e32 v223, 1.0, v223
	v_rcp_f32_e32 v220, v254
	v_add_f32_e32 v224, 1.0, v224
	v_mfma_f32_32x32x16_bf16 v[18:33], v[62:65], v[146:149], v[18:33]
	v_rcp_f32_e32 v221, v221
	v_fma_f32 v240, -v212, v217, v217
	v_rcp_f32_e32 v222, v222
	v_fma_f32 v241, -v213, v218, v218
	v_rcp_f32_e32 v223, v223
	v_fma_f32 v242, -v214, v219, v219
	v_rcp_f32_e32 v224, v224
	v_fma_f32 v243, -v215, v220, v220
	v_mfma_f32_32x32x16_bf16 v[18:33], v[58:61], v[150:153], v[18:33]
	v_exp_f32_e32 v246, v5
	v_fma_f32 v194, v221, v194, v240
	v_exp_f32_e32 v247, v9
	v_fma_f32 v195, v222, v195, v241
	v_exp_f32_e32 v248, v13
	v_fma_f32 v196, v223, v196, v242
	v_exp_f32_e32 v249, v17
	v_fma_f32 v197, v224, v197, v243
	v_mfma_f32_32x32x16_bf16 v[18:33], v[54:57], v[154:157], v[18:33]
	v_exp_f32_e32 v212, v194
	v_add_f32_e32 v246, 1.0, v246
	v_exp_f32_e32 v213, v195
	v_add_f32_e32 v247, 1.0, v247
	v_exp_f32_e32 v214, v196
	v_add_f32_e32 v248, 1.0, v248
	v_exp_f32_e32 v215, v197
	v_add_f32_e32 v249, 1.0, v249
	v_fmac_f32_e32 v246, v246, v212
	v_fmac_f32_e32 v247, v247, v213
	v_fmac_f32_e32 v248, v248, v214
	v_fmac_f32_e32 v249, v249, v215
	v_mfma_f32_32x32x16_bf16 v[18:33], v[50:53], v[158:161], v[18:33]
	v_rcp_f32_e32 v246, v246
	v_rcp_f32_e32 v247, v247
	v_rcp_f32_e32 v248, v248
	v_rcp_f32_e32 v249, v249
	v_fma_f32 v246, -v212, v246, v246
	v_fma_f32 v247, -v213, v247, v247
	v_fma_f32 v248, -v214, v248, v248
	v_fma_f32 v249, -v215, v249, v249
	v_cvt_pk_bf16_f32 v236, v246, v247
	v_cvt_pk_bf16_f32 v237, v248, v249
	s_waitcnt lgkmcnt(0)
	v_mfma_f32_32x32x16_bf16 v[34:49], v[126:129], v[162:165], v[34:49]
	v_exp_f32_e32 v212, v20
	v_exp_f32_e32 v213, v24
	v_exp_f32_e32 v214, v28
	v_exp_f32_e32 v215, v32
	v_mfma_f32_32x32x16_bf16 v[34:49], v[122:125], v[166:169], v[34:49]
	v_exp_f32_e32 v217, v18
	v_fma_f32 v251, v212, s12, s12
	v_exp_f32_e32 v218, v22
	v_fma_f32 v252, v213, s12, s12
	v_exp_f32_e32 v219, v26
	v_fma_f32 v253, v214, s12, s12
	v_exp_f32_e32 v220, v30
	v_fma_f32 v254, v215, s12, s12
	v_mfma_f32_32x32x16_bf16 v[34:49], v[118:121], v[170:173], v[34:49]
	v_exp_f32_e32 v221, v19
	v_fmac_f32_e32 v251, v217, v251
	v_exp_f32_e32 v222, v23
	v_fmac_f32_e32 v252, v218, v252
	v_exp_f32_e32 v223, v27
	v_fmac_f32_e32 v253, v219, v253
	v_exp_f32_e32 v224, v31
	v_fmac_f32_e32 v254, v220, v254
	v_mfma_f32_32x32x16_bf16 v[34:49], v[114:117], v[174:177], v[34:49]
	v_rcp_f32_e32 v217, v251
	v_add_f32_e32 v221, 1.0, v221
	v_rcp_f32_e32 v218, v252
	v_add_f32_e32 v222, 1.0, v222
	v_rcp_f32_e32 v219, v253
	v_add_f32_e32 v223, 1.0, v223
	v_rcp_f32_e32 v220, v254
	v_add_f32_e32 v224, 1.0, v224
	v_mfma_f32_32x32x16_bf16 v[34:49], v[110:113], v[178:181], v[34:49]
	v_rcp_f32_e32 v221, v221
	v_fma_f32 v240, -v212, v217, v217
	v_rcp_f32_e32 v222, v222
	v_fma_f32 v241, -v213, v218, v218
	v_rcp_f32_e32 v223, v223
	v_fma_f32 v242, -v214, v219, v219
	v_rcp_f32_e32 v224, v224
	v_fma_f32 v243, -v215, v220, v220
	v_mfma_f32_32x32x16_bf16 v[34:49], v[106:109], v[182:185], v[34:49]
	v_exp_f32_e32 v246, v21
	v_fma_f32 v198, v221, v198, v240
	v_exp_f32_e32 v247, v25
	v_fma_f32 v199, v222, v199, v241
	v_exp_f32_e32 v248, v29
	v_fma_f32 v200, v223, v200, v242
	v_exp_f32_e32 v249, v33
	v_fma_f32 v201, v224, v201, v243
	v_mfma_f32_32x32x16_bf16 v[34:49], v[102:105], v[186:189], v[34:49]
	v_exp_f32_e32 v212, v198
	v_add_f32_e32 v246, 1.0, v246
	v_exp_f32_e32 v213, v199
	v_add_f32_e32 v247, 1.0, v247
	v_exp_f32_e32 v214, v200
	v_add_f32_e32 v248, 1.0, v248
	v_exp_f32_e32 v215, v201
	v_add_f32_e32 v249, 1.0, v249
	v_fmac_f32_e32 v246, v246, v212
	v_fmac_f32_e32 v247, v247, v213
	v_fmac_f32_e32 v248, v248, v214
	v_fmac_f32_e32 v249, v249, v215
	v_mfma_f32_32x32x16_bf16 v[34:49], v[98:101], v[190:193], v[34:49]
	v_rcp_f32_e32 v246, v246
	v_rcp_f32_e32 v247, v247
	v_rcp_f32_e32 v248, v248
	v_rcp_f32_e32 v249, v249
	v_fma_f32 v246, -v212, v246, v246
	v_fma_f32 v247, -v213, v247, v247
	v_fma_f32 v248, -v214, v248, v248
	v_fma_f32 v249, -v215, v249, v249
	v_cvt_pk_bf16_f32 v238, v246, v247
	v_cvt_pk_bf16_f32 v239, v248, v249
	ds_write_b128 v211, v[236:239] offset:0
	s_waitcnt lgkmcnt(0)
	s_barrier
	s_bfe_u32 s20, s19, 0x10006
	s_lshl_b32 s21, s20, 7
	s_lshl_b32 s20, s20, 13
	s_add_u32 s20, s20, 0x30000
	s_add_u32 s22, s14, s20
	s_addc_u32 s23, s15, 0
	s_add_u32 s24, s22, 0x1000
	s_addc_u32 s25, s23, 0
	global_load_dwordx4 v[130:133], v210, s[22:23] offset:0
	global_load_dwordx4 v[130:133], v210, s[22:23] offset:1024
	global_load_dwordx4 v[130:133], v210, s[22:23] offset:2048
	global_load_dwordx4 v[130:133], v210, s[22:23] offset:3072
	global_load_dwordx4 v[130:133], v210, s[24:25] offset:0
	global_load_dwordx4 v[130:133], v210, s[24:25] offset:1024
	global_load_dwordx4 v[130:133], v210, s[24:25] offset:2048
	global_load_dwordx4 v[130:133], v210, s[24:25] offset:3072
	v_or_b32_e32 v138, s21, v230
	global_load_dwordx4 v[134:137], v138, s[4:5] offset:0
	global_load_dwordx4 v[134:137], v138, s[4:5] offset:32
	global_load_dwordx4 v[134:137], v138, s[4:5] offset:64
	global_load_dwordx4 v[134:137], v138, s[4:5] offset:96
	global_load_dwordx4 v[134:137], v138, s[6:7] offset:0
	global_load_dwordx4 v[134:137], v138, s[6:7] offset:32
	global_load_dwordx4 v[134:137], v138, s[6:7] offset:64
	global_load_dwordx4 v[134:137], v138, s[6:7] offset:96
	s_load_dword s21, s[8:9], 0x0
	v_mfma_f32_32x32x16_bf16 v[82:97], v[78:81], v[162:165], v[82:97]
	v_exp_f32_e32 v212, v36
	v_exp_f32_e32 v213, v40
	v_exp_f32_e32 v214, v44
	v_exp_f32_e32 v215, v48
	v_mfma_f32_32x32x16_bf16 v[82:97], v[74:77], v[166:169], v[82:97]
	v_exp_f32_e32 v217, v34
	v_fma_f32 v251, v212, s12, s12
	v_exp_f32_e32 v218, v38
	v_fma_f32 v252, v213, s12, s12
	v_exp_f32_e32 v219, v42
	v_fma_f32 v253, v214, s12, s12
	v_exp_f32_e32 v220, v46
	v_fma_f32 v254, v215, s12, s12
	v_mfma_f32_32x32x16_bf16 v[82:97], v[70:73], v[170:173], v[82:97]
	v_exp_f32_e32 v221, v35
	v_fmac_f32_e32 v251, v217, v251
	v_exp_f32_e32 v222, v39
	v_fmac_f32_e32 v252, v218, v252
	v_exp_f32_e32 v223, v43
	v_fmac_f32_e32 v253, v219, v253
	v_exp_f32_e32 v224, v47
	v_fmac_f32_e32 v254, v220, v254
	v_mfma_f32_32x32x16_bf16 v[82:97], v[66:69], v[174:177], v[82:97]
	v_rcp_f32_e32 v217, v251
	v_add_f32_e32 v221, 1.0, v221
	v_rcp_f32_e32 v218, v252
	v_add_f32_e32 v222, 1.0, v222
	v_rcp_f32_e32 v219, v253
	v_add_f32_e32 v223, 1.0, v223
	v_rcp_f32_e32 v220, v254
	v_add_f32_e32 v224, 1.0, v224
	v_mfma_f32_32x32x16_bf16 v[82:97], v[62:65], v[178:181], v[82:97]
	v_rcp_f32_e32 v221, v221
	v_fma_f32 v240, -v212, v217, v217
	v_rcp_f32_e32 v222, v222
	v_fma_f32 v241, -v213, v218, v218
	v_rcp_f32_e32 v223, v223
	v_fma_f32 v242, -v214, v219, v219
	v_rcp_f32_e32 v224, v224
	v_fma_f32 v243, -v215, v220, v220
	v_mfma_f32_32x32x16_bf16 v[82:97], v[58:61], v[182:185], v[82:97]
	v_exp_f32_e32 v246, v37
	v_fma_f32 v202, v221, v202, v240
	v_exp_f32_e32 v247, v41
	v_fma_f32 v203, v222, v203, v241
	v_exp_f32_e32 v248, v45
	v_fma_f32 v204, v223, v204, v242
	v_exp_f32_e32 v249, v49
	v_fma_f32 v205, v224, v205, v243
	v_mfma_f32_32x32x16_bf16 v[82:97], v[54:57], v[186:189], v[82:97]
	v_exp_f32_e32 v212, v202
	v_add_f32_e32 v246, 1.0, v246
	v_exp_f32_e32 v213, v203
	v_add_f32_e32 v247, 1.0, v247
	v_exp_f32_e32 v214, v204
	v_add_f32_e32 v248, 1.0, v248
	v_exp_f32_e32 v215, v205
	v_add_f32_e32 v249, 1.0, v249
	v_fmac_f32_e32 v246, v246, v212
	v_fmac_f32_e32 v247, v247, v213
	v_fmac_f32_e32 v248, v248, v214
	v_fmac_f32_e32 v249, v249, v215
	v_mfma_f32_32x32x16_bf16 v[82:97], v[50:53], v[190:193], v[82:97]
	v_rcp_f32_e32 v246, v246
	v_rcp_f32_e32 v247, v247
	v_rcp_f32_e32 v248, v248
	v_rcp_f32_e32 v249, v249
	v_fma_f32 v246, -v212, v246, v246
	v_fma_f32 v247, -v213, v247, v247
	v_fma_f32 v248, -v214, v248, v248
	v_fma_f32 v249, -v215, v249, v249
	v_cvt_pk_bf16_f32 v236, v246, v247
	v_cvt_pk_bf16_f32 v237, v248, v249
	s_waitcnt lgkmcnt(0)
	v_exp_f32_e32 v212, v84
	v_exp_f32_e32 v213, v88
	v_exp_f32_e32 v214, v92
	v_exp_f32_e32 v215, v96
	v_exp_f32_e32 v217, v82
	v_fma_f32 v251, v212, s12, s12
	v_exp_f32_e32 v218, v86
	v_fma_f32 v252, v213, s12, s12
	v_exp_f32_e32 v219, v90
	v_fma_f32 v253, v214, s12, s12
	v_exp_f32_e32 v220, v94
	v_fma_f32 v254, v215, s12, s12
	v_exp_f32_e32 v221, v83
	v_fmac_f32_e32 v251, v217, v251
	v_exp_f32_e32 v222, v87
	v_fmac_f32_e32 v252, v218, v252
	v_exp_f32_e32 v223, v91
	v_fmac_f32_e32 v253, v219, v253
	v_exp_f32_e32 v224, v95
	v_fmac_f32_e32 v254, v220, v254
	v_rcp_f32_e32 v217, v251
	v_add_f32_e32 v221, 1.0, v221
	v_rcp_f32_e32 v218, v252
	v_add_f32_e32 v222, 1.0, v222
	v_rcp_f32_e32 v219, v253
	v_add_f32_e32 v223, 1.0, v223
	v_rcp_f32_e32 v220, v254
	v_add_f32_e32 v224, 1.0, v224
	v_rcp_f32_e32 v221, v221
	v_fma_f32 v240, -v212, v217, v217
	v_rcp_f32_e32 v222, v222
	v_fma_f32 v241, -v213, v218, v218
	v_rcp_f32_e32 v223, v223
	v_fma_f32 v242, -v214, v219, v219
	v_rcp_f32_e32 v224, v224
	v_fma_f32 v243, -v215, v220, v220
	v_exp_f32_e32 v246, v85
	v_fma_f32 v206, v221, v206, v240
	v_exp_f32_e32 v247, v89
	v_fma_f32 v207, v222, v207, v241
	v_exp_f32_e32 v248, v93
	v_fma_f32 v208, v223, v208, v242
	v_exp_f32_e32 v249, v97
	v_fma_f32 v209, v224, v209, v243
	v_exp_f32_e32 v212, v206
	v_add_f32_e32 v246, 1.0, v246
	v_exp_f32_e32 v213, v207
	v_add_f32_e32 v247, 1.0, v247
	v_exp_f32_e32 v214, v208
	v_add_f32_e32 v248, 1.0, v248
	v_exp_f32_e32 v215, v209
	v_add_f32_e32 v249, 1.0, v249
	v_fmac_f32_e32 v246, v246, v212
	v_fmac_f32_e32 v247, v247, v213
	v_fmac_f32_e32 v248, v248, v214
	v_fmac_f32_e32 v249, v249, v215
	v_rcp_f32_e32 v246, v246
	v_rcp_f32_e32 v247, v247
	v_rcp_f32_e32 v248, v248
	v_rcp_f32_e32 v249, v249
	v_fma_f32 v246, -v212, v246, v246
	v_fma_f32 v247, -v213, v247, v247
	v_fma_f32 v248, -v214, v248, v248
	v_fma_f32 v249, -v215, v249, v249
	v_cvt_pk_bf16_f32 v238, v246, v247
	v_cvt_pk_bf16_f32 v239, v248, v249
	ds_write_b128 v211, v[236:239] offset:8192
	s_waitcnt lgkmcnt(0)
	s_barrier
	s_waitcnt vmcnt(0)
	s_nop 7
	s_nop 7
	s_branch .Lepilogue
